# GEMM K-loops: pointer/m0 bookkeeping spread between the MFMAs instead of behind the closing barrier (on top of edge trimming and shadowed A-fragment reads)
# baseline (speedup 1.0000x reference)
.LBB0_267:
	s_add_u32 s16, s14, 0x80
	s_addc_u32 s17, s15, 0
	s_add_i32 s41, 0, 0x10000
	v_add_u32_e32 v144, s41, v147
	ds_read_b128 v[150:153], v144
	ds_read_b128 v[154:157], v144 offset:1024
	ds_read_b128 v[158:161], v144 offset:2048
	ds_read_b128 v[162:165], v144 offset:3072
	s_cmp_eq_u32 s40, 28
	s_cselect_b32 s19, s11, s17
	s_cselect_b32 s18, s10, s16
	s_cselect_b32 s17, s13, s39
	s_cselect_b32 s16, s12, s38
	v_lshl_add_u64 v[144:145], s[14:15], 0, v[142:143]
	s_add_i32 m0, s27, 0xc000
	s_nop 0
	global_load_lds_dwordx4 v[144:145], off
	v_lshl_add_u64 v[144:145], s[14:15], 0, v[140:141]
	s_add_i32 m0, s27, 0xe000
	s_nop 0
	global_load_lds_dwordx4 v[144:145], off
	s_waitcnt lgkmcnt(0)
	s_setprio 1
	s_barrier
	s_waitcnt lgkmcnt(0)
	v_mfma_f32_16x16x32_bf16 v[124:127], v[150:153], v[172:175], v[124:127]
	v_mfma_f32_16x16x32_bf16 v[120:123], v[158:161], v[172:175], v[120:123]
	v_mfma_f32_16x16x32_bf16 v[116:119], v[150:153], v[180:183], v[116:119]
	v_mfma_f32_16x16x32_bf16 v[108:111], v[158:161], v[180:183], v[108:111]
	v_mfma_f32_16x16x32_bf16 v[100:103], v[150:153], v[212:215], v[100:103]
	v_mfma_f32_16x16x32_bf16 v[92:95], v[158:161], v[212:215], v[92:95]
	v_mfma_f32_16x16x32_bf16 v[84:87], v[150:153], v[220:223], v[84:87]
	v_mfma_f32_16x16x32_bf16 v[76:79], v[158:161], v[220:223], v[76:79]
	v_mfma_f32_16x16x32_bf16 v[124:127], v[154:157], v[176:179], v[124:127]
	v_mfma_f32_16x16x32_bf16 v[120:123], v[162:165], v[176:179], v[120:123]
	v_mfma_f32_16x16x32_bf16 v[116:119], v[154:157], v[208:211], v[116:119]
	v_mfma_f32_16x16x32_bf16 v[108:111], v[162:165], v[208:211], v[108:111]
	v_mfma_f32_16x16x32_bf16 v[100:103], v[154:157], v[216:219], v[100:103]
	v_mfma_f32_16x16x32_bf16 v[92:95], v[162:165], v[216:219], v[92:95]
	v_mfma_f32_16x16x32_bf16 v[84:87], v[154:157], v[224:227], v[84:87]
	v_mfma_f32_16x16x32_bf16 v[76:79], v[162:165], v[224:227], v[76:79]
	s_barrier
	s_setprio 0
	s_add_i32 s44, 0, 0x14000
	v_add_u32_e32 v144, s44, v147
	s_add_i32 s41, s41, s25
	ds_read_b128 v[228:231], v144
	ds_read_b128 v[232:235], v144 offset:1024
	ds_read_b128 v[236:239], v144 offset:2048
	ds_read_b128 v[240:243], v144 offset:3072
	v_lshl_add_u64 v[144:145], s[16:17], 0, v[138:139]
	s_mov_b32 m0, s41
	v_lshl_add_u64 v[166:167], s[16:17], 0, v[132:133]
	global_load_lds_dwordx4 v[144:145], off
	s_add_i32 m0, s41, 0x2000
	s_nop 0
	global_load_lds_dwordx4 v[166:167], off
	s_setprio 1
	s_barrier
	s_waitcnt lgkmcnt(0)
	v_mfma_f32_16x16x32_bf16 v[112:115], v[228:231], v[172:175], v[112:115]
	s_mov_b32 m0, s27
	v_mfma_f32_16x16x32_bf16 v[104:107], v[236:239], v[172:175], v[104:107]
	v_lshl_add_u64 v[184:185], s[18:19], 0, v[134:135]
	ds_read_b128 v[172:175], v148 offset:16384
	v_mfma_f32_16x16x32_bf16 v[96:99], v[228:231], v[180:183], v[96:99]
	v_mfma_f32_16x16x32_bf16 v[88:91], v[236:239], v[180:183], v[88:91]
	ds_read_b128 v[180:183], v148 offset:18432
	v_mfma_f32_16x16x32_bf16 v[80:83], v[228:231], v[212:215], v[80:83]
	v_mfma_f32_16x16x32_bf16 v[72:75], v[236:239], v[212:215], v[72:75]
	ds_read_b128 v[212:215], v148 offset:20480
	v_mfma_f32_16x16x32_bf16 v[68:71], v[228:231], v[220:223], v[68:71]
	v_mfma_f32_16x16x32_bf16 v[64:67], v[236:239], v[220:223], v[64:67]
	ds_read_b128 v[220:223], v148 offset:22528
	v_mfma_f32_16x16x32_bf16 v[112:115], v[232:235], v[176:179], v[112:115]
	v_mfma_f32_16x16x32_bf16 v[104:107], v[240:243], v[176:179], v[104:107]
	ds_read_b128 v[176:179], v148 offset:17408
	v_mfma_f32_16x16x32_bf16 v[96:99], v[232:235], v[208:211], v[96:99]
	v_mfma_f32_16x16x32_bf16 v[88:91], v[240:243], v[208:211], v[88:91]
	ds_read_b128 v[208:211], v148 offset:19456
	v_mfma_f32_16x16x32_bf16 v[80:83], v[232:235], v[216:219], v[80:83]
	v_mfma_f32_16x16x32_bf16 v[72:75], v[240:243], v[216:219], v[72:75]
	ds_read_b128 v[216:219], v148 offset:21504
	v_mfma_f32_16x16x32_bf16 v[68:71], v[232:235], v[224:227], v[68:71]
	v_mfma_f32_16x16x32_bf16 v[64:67], v[240:243], v[224:227], v[64:67]
	ds_read_b128 v[224:227], v148 offset:23552
	s_barrier
	s_setprio 0
	global_load_lds_dwordx4 v[184:185], off
	v_lshl_add_u64 v[244:245], s[18:19], 0, v[128:129]
	s_mov_b32 m0, s28
	s_nop 0
	global_load_lds_dwordx4 v[244:245], off
	s_waitcnt vmcnt(8)
	s_setprio 1
	s_barrier
	s_waitcnt lgkmcnt(0)
	v_mfma_f32_16x16x32_bf16 v[60:63], v[150:153], v[172:175], v[60:63]
	v_mfma_f32_16x16x32_bf16 v[56:59], v[158:161], v[172:175], v[56:59]
	v_mfma_f32_16x16x32_bf16 v[44:47], v[150:153], v[180:183], v[44:47]
	v_mfma_f32_16x16x32_bf16 v[36:39], v[158:161], v[180:183], v[36:39]
	v_mfma_f32_16x16x32_bf16 v[20:23], v[150:153], v[212:215], v[20:23]
	v_mfma_f32_16x16x32_bf16 v[12:15], v[158:161], v[212:215], v[12:15]
	v_mfma_f32_16x16x32_bf16 v[4:7], v[150:153], v[220:223], v[4:7]
	v_mfma_f32_16x16x32_bf16 v[0:3], v[158:161], v[220:223], v[0:3]
	v_mfma_f32_16x16x32_bf16 v[60:63], v[154:157], v[176:179], v[60:63]
	v_mfma_f32_16x16x32_bf16 v[56:59], v[162:165], v[176:179], v[56:59]
	v_mfma_f32_16x16x32_bf16 v[44:47], v[154:157], v[208:211], v[44:47]
	v_mfma_f32_16x16x32_bf16 v[36:39], v[162:165], v[208:211], v[36:39]
	v_mfma_f32_16x16x32_bf16 v[20:23], v[154:157], v[216:219], v[20:23]
	v_mfma_f32_16x16x32_bf16 v[12:15], v[162:165], v[216:219], v[12:15]
	v_mfma_f32_16x16x32_bf16 v[4:7], v[154:157], v[224:227], v[4:7]
	v_mfma_f32_16x16x32_bf16 v[0:3], v[162:165], v[224:227], v[0:3]
	s_barrier
	s_setprio 0
	s_add_u32 s42, s16, 0x80000
	s_addc_u32 s43, s17, 0
	s_add_i32 s41, s44, s25
	v_lshl_add_u64 v[150:151], s[42:43], 0, v[138:139]
	s_mov_b32 m0, s41
	s_nop 0
	global_load_lds_dwordx4 v[150:151], off
	v_lshl_add_u64 v[150:151], s[42:43], 0, v[132:133]
	s_add_i32 m0, s41, 0x2000
	s_nop 0
	global_load_lds_dwordx4 v[150:151], off
	s_waitcnt vmcnt(6)
	s_setprio 1
	s_barrier
	v_mfma_f32_16x16x32_bf16 v[40:43], v[228:231], v[172:175], v[40:43]
	s_add_i32 s41, 0, 0x18000
	v_mfma_f32_16x16x32_bf16 v[28:31], v[236:239], v[172:175], v[28:31]
	v_add_u32_e32 v149, s41, v147
	ds_read_b128 v[172:175], v148 offset:32768
	v_mfma_f32_16x16x32_bf16 v[16:19], v[228:231], v[180:183], v[16:19]
	v_mfma_f32_16x16x32_bf16 v[8:11], v[236:239], v[180:183], v[8:11]
	ds_read_b128 v[180:183], v148 offset:34816
	v_mfma_f32_16x16x32_bf16 v[52:55], v[228:231], v[212:215], v[52:55]
	v_mfma_f32_16x16x32_bf16 v[48:51], v[236:239], v[212:215], v[48:51]
	ds_read_b128 v[212:215], v148 offset:36864
	v_mfma_f32_16x16x32_bf16 v[32:35], v[228:231], v[220:223], v[32:35]
	v_mfma_f32_16x16x32_bf16 v[24:27], v[236:239], v[220:223], v[24:27]
	ds_read_b128 v[220:223], v148 offset:38912
	v_mfma_f32_16x16x32_bf16 v[40:43], v[232:235], v[176:179], v[40:43]
	v_mfma_f32_16x16x32_bf16 v[28:31], v[240:243], v[176:179], v[28:31]
	ds_read_b128 v[176:179], v148 offset:33792
	v_mfma_f32_16x16x32_bf16 v[16:19], v[232:235], v[208:211], v[16:19]
	v_mfma_f32_16x16x32_bf16 v[8:11], v[240:243], v[208:211], v[8:11]
	ds_read_b128 v[208:211], v148 offset:35840
	v_mfma_f32_16x16x32_bf16 v[52:55], v[232:235], v[216:219], v[52:55]
	v_mfma_f32_16x16x32_bf16 v[48:51], v[240:243], v[216:219], v[48:51]
	ds_read_b128 v[216:219], v148 offset:37888
	v_mfma_f32_16x16x32_bf16 v[32:35], v[232:235], v[224:227], v[32:35]
	v_mfma_f32_16x16x32_bf16 v[24:27], v[240:243], v[224:227], v[24:27]
	ds_read_b128 v[224:227], v148 offset:39936
	s_barrier
	s_setprio 0
	ds_read_b128 v[150:153], v149
	ds_read_b128 v[154:157], v149 offset:1024
	ds_read_b128 v[158:161], v149 offset:2048
	ds_read_b128 v[162:165], v149 offset:3072
	s_mov_b32 m0, s29
	v_lshl_add_u64 v[228:229], s[18:19], 0, v[136:137]
	global_load_lds_dwordx4 v[228:229], off
	v_lshl_add_u64 v[228:229], s[18:19], 0, v[130:131]
	s_mov_b32 m0, s30
	s_nop 0
	global_load_lds_dwordx4 v[228:229], off
	s_waitcnt lgkmcnt(0)
	s_setprio 1
	s_barrier
	s_waitcnt lgkmcnt(0)
	v_mfma_f32_16x16x32_bf16 v[124:127], v[150:153], v[172:175], v[124:127]
	v_mfma_f32_16x16x32_bf16 v[120:123], v[158:161], v[172:175], v[120:123]
	v_mfma_f32_16x16x32_bf16 v[116:119], v[150:153], v[180:183], v[116:119]
	v_mfma_f32_16x16x32_bf16 v[108:111], v[158:161], v[180:183], v[108:111]
	v_mfma_f32_16x16x32_bf16 v[100:103], v[150:153], v[212:215], v[100:103]
	v_mfma_f32_16x16x32_bf16 v[92:95], v[158:161], v[212:215], v[92:95]
	v_mfma_f32_16x16x32_bf16 v[84:87], v[150:153], v[220:223], v[84:87]
	v_mfma_f32_16x16x32_bf16 v[76:79], v[158:161], v[220:223], v[76:79]
	v_mfma_f32_16x16x32_bf16 v[124:127], v[154:157], v[176:179], v[124:127]
	v_mfma_f32_16x16x32_bf16 v[120:123], v[162:165], v[176:179], v[120:123]
	v_mfma_f32_16x16x32_bf16 v[116:119], v[154:157], v[208:211], v[116:119]
	v_mfma_f32_16x16x32_bf16 v[108:111], v[162:165], v[208:211], v[108:111]
	v_mfma_f32_16x16x32_bf16 v[100:103], v[154:157], v[216:219], v[100:103]
	v_mfma_f32_16x16x32_bf16 v[92:95], v[162:165], v[216:219], v[92:95]
	v_mfma_f32_16x16x32_bf16 v[84:87], v[154:157], v[224:227], v[84:87]
	v_mfma_f32_16x16x32_bf16 v[76:79], v[162:165], v[224:227], v[76:79]
	s_barrier
	s_setprio 0
	s_add_i32 s18, 0, 0x1c000
	s_add_i32 s19, s41, s25
	v_add_u32_e32 v149, s18, v147
	v_lshl_add_u64 v[144:145], v[144:145], 0, s[94:95]
	s_mov_b32 m0, s19
	ds_read_b128 v[228:231], v149
	ds_read_b128 v[232:235], v149 offset:1024
	ds_read_b128 v[236:239], v149 offset:2048
	ds_read_b128 v[240:243], v149 offset:3072
	global_load_lds_dwordx4 v[144:145], off
	v_lshl_add_u64 v[144:145], v[166:167], 0, s[94:95]
	s_add_i32 m0, s19, 0x2000
	s_nop 0
	global_load_lds_dwordx4 v[144:145], off
	s_setprio 1
	s_barrier
	s_waitcnt lgkmcnt(0)
	v_mfma_f32_16x16x32_bf16 v[112:115], v[228:231], v[172:175], v[112:115]
	s_mov_b32 m0, s31
	v_mfma_f32_16x16x32_bf16 v[104:107], v[236:239], v[172:175], v[104:107]
	v_lshl_add_u64 v[144:145], v[184:185], 0, s[94:95]
	ds_read_b128 v[172:175], v148 offset:49152
	v_mfma_f32_16x16x32_bf16 v[96:99], v[228:231], v[180:183], v[96:99]
	v_mfma_f32_16x16x32_bf16 v[88:91], v[236:239], v[180:183], v[88:91]
	ds_read_b128 v[180:183], v148 offset:51200
	v_mfma_f32_16x16x32_bf16 v[80:83], v[228:231], v[212:215], v[80:83]
	v_mfma_f32_16x16x32_bf16 v[72:75], v[236:239], v[212:215], v[72:75]
	ds_read_b128 v[212:215], v148 offset:53248
	v_mfma_f32_16x16x32_bf16 v[68:71], v[228:231], v[220:223], v[68:71]
	v_mfma_f32_16x16x32_bf16 v[64:67], v[236:239], v[220:223], v[64:67]
	ds_read_b128 v[220:223], v148 offset:55296
	v_mfma_f32_16x16x32_bf16 v[112:115], v[232:235], v[176:179], v[112:115]
	v_mfma_f32_16x16x32_bf16 v[104:107], v[240:243], v[176:179], v[104:107]
	ds_read_b128 v[176:179], v148 offset:50176
	v_mfma_f32_16x16x32_bf16 v[96:99], v[232:235], v[208:211], v[96:99]
	v_mfma_f32_16x16x32_bf16 v[88:91], v[240:243], v[208:211], v[88:91]
	ds_read_b128 v[208:211], v148 offset:52224
	v_mfma_f32_16x16x32_bf16 v[80:83], v[232:235], v[216:219], v[80:83]
	v_mfma_f32_16x16x32_bf16 v[72:75], v[240:243], v[216:219], v[72:75]
	ds_read_b128 v[216:219], v148 offset:54272
	v_mfma_f32_16x16x32_bf16 v[68:71], v[232:235], v[224:227], v[68:71]
	v_mfma_f32_16x16x32_bf16 v[64:67], v[240:243], v[224:227], v[64:67]
	ds_read_b128 v[224:227], v148 offset:56320
	s_barrier
	s_setprio 0
	global_load_lds_dwordx4 v[144:145], off
	v_lshl_add_u64 v[144:145], v[244:245], 0, s[94:95]
	s_mov_b32 m0, s34
	s_nop 0
	global_load_lds_dwordx4 v[144:145], off
	s_waitcnt vmcnt(8)
	s_setprio 1
	s_barrier
	s_waitcnt lgkmcnt(0)
	v_mfma_f32_16x16x32_bf16 v[60:63], v[150:153], v[172:175], v[60:63]
	v_mfma_f32_16x16x32_bf16 v[56:59], v[158:161], v[172:175], v[56:59]
	v_mfma_f32_16x16x32_bf16 v[44:47], v[150:153], v[180:183], v[44:47]
	v_mfma_f32_16x16x32_bf16 v[36:39], v[158:161], v[180:183], v[36:39]
	v_mfma_f32_16x16x32_bf16 v[20:23], v[150:153], v[212:215], v[20:23]
	v_mfma_f32_16x16x32_bf16 v[12:15], v[158:161], v[212:215], v[12:15]
	v_mfma_f32_16x16x32_bf16 v[4:7], v[150:153], v[220:223], v[4:7]
	v_mfma_f32_16x16x32_bf16 v[0:3], v[158:161], v[220:223], v[0:3]
	v_mfma_f32_16x16x32_bf16 v[60:63], v[154:157], v[176:179], v[60:63]
	v_mfma_f32_16x16x32_bf16 v[56:59], v[162:165], v[176:179], v[56:59]
	v_mfma_f32_16x16x32_bf16 v[44:47], v[154:157], v[208:211], v[44:47]
	v_mfma_f32_16x16x32_bf16 v[36:39], v[162:165], v[208:211], v[36:39]
	v_mfma_f32_16x16x32_bf16 v[20:23], v[154:157], v[216:219], v[20:23]
	v_mfma_f32_16x16x32_bf16 v[12:15], v[162:165], v[216:219], v[12:15]
	v_mfma_f32_16x16x32_bf16 v[4:7], v[154:157], v[224:227], v[4:7]
	v_mfma_f32_16x16x32_bf16 v[0:3], v[162:165], v[224:227], v[0:3]
	s_barrier
	s_setprio 0
	s_add_u32 s16, s16, 0x80080
	s_addc_u32 s17, s17, 0
	s_add_i32 s18, s18, s25
	v_lshl_add_u64 v[144:145], s[16:17], 0, v[138:139]
	s_mov_b32 m0, s18
	s_nop 0
	global_load_lds_dwordx4 v[144:145], off
	v_lshl_add_u64 v[144:145], s[16:17], 0, v[132:133]
	s_add_i32 m0, s18, 0x2000
	s_nop 0
	global_load_lds_dwordx4 v[144:145], off
	s_waitcnt vmcnt(6)
	s_setprio 1
	s_barrier
	v_mfma_f32_16x16x32_bf16 v[40:43], v[228:231], v[172:175], v[40:43]
	s_add_i32 s40, s40, 2
	v_mfma_f32_16x16x32_bf16 v[28:31], v[236:239], v[172:175], v[28:31]
	s_add_u32 s14, s14, 0x100
	ds_read_b128 v[172:175], v148
	v_mfma_f32_16x16x32_bf16 v[16:19], v[228:231], v[180:183], v[16:19]
	s_addc_u32 s15, s15, 0
	v_mfma_f32_16x16x32_bf16 v[8:11], v[236:239], v[180:183], v[8:11]
	s_add_u32 s38, s38, 0x100
	ds_read_b128 v[180:183], v148 offset:2048
	v_mfma_f32_16x16x32_bf16 v[52:55], v[228:231], v[212:215], v[52:55]
	s_addc_u32 s39, s39, 0
	v_mfma_f32_16x16x32_bf16 v[48:51], v[236:239], v[212:215], v[48:51]
	s_cmp_gt_u32 s40, 29
	ds_read_b128 v[212:215], v148 offset:4096
	v_mfma_f32_16x16x32_bf16 v[32:35], v[228:231], v[220:223], v[32:35]
	v_mfma_f32_16x16x32_bf16 v[24:27], v[236:239], v[220:223], v[24:27]
	ds_read_b128 v[220:223], v148 offset:6144
	v_mfma_f32_16x16x32_bf16 v[40:43], v[232:235], v[176:179], v[40:43]
	v_mfma_f32_16x16x32_bf16 v[28:31], v[240:243], v[176:179], v[28:31]
	ds_read_b128 v[176:179], v148 offset:1024
	v_mfma_f32_16x16x32_bf16 v[16:19], v[232:235], v[208:211], v[16:19]
	v_mfma_f32_16x16x32_bf16 v[8:11], v[240:243], v[208:211], v[8:11]
	ds_read_b128 v[208:211], v148 offset:3072
	v_mfma_f32_16x16x32_bf16 v[52:55], v[232:235], v[216:219], v[52:55]
	v_mfma_f32_16x16x32_bf16 v[48:51], v[240:243], v[216:219], v[48:51]
	ds_read_b128 v[216:219], v148 offset:5120
	v_mfma_f32_16x16x32_bf16 v[32:35], v[232:235], v[224:227], v[32:35]
	v_mfma_f32_16x16x32_bf16 v[24:27], v[240:243], v[224:227], v[24:27]
	ds_read_b128 v[224:227], v148 offset:7168
	s_barrier
	s_setprio 0
	s_cbranch_scc0 .LBB0_267
	s_waitcnt lgkmcnt(0)
	s_and_b64 vcc, exec, s[6:7]
	s_cbranch_vccz .LBB0_270
	s_barrier

.LBB0_424:
	s_add_u32 s12, s10, 0x3200
	s_addc_u32 s13, s11, 0
	s_add_i32 s38, 0, 0x10000
	v_add_u32_e32 v147, s38, v145
	ds_read_b128 v[148:151], v147
	ds_read_b128 v[152:155], v147 offset:1024
	ds_read_b128 v[156:159], v147 offset:2048
	ds_read_b128 v[160:163], v147 offset:3072
	s_cmp_eq_u32 s37, 12
	s_cselect_b32 s17, s5, s13
	s_cselect_b32 s16, s4, s12
	s_cselect_b32 s15, s7, s36
	s_cselect_b32 s14, s6, s35
	v_lshl_add_u64 v[184:185], s[10:11], 0, v[142:143]
	s_add_i32 m0, s24, 0xc000
	ds_read_b128 v[164:167], v146
	ds_read_b128 v[172:175], v146 offset:1024
	ds_read_b128 v[176:179], v146 offset:2048
	ds_read_b128 v[180:183], v146 offset:3072
	ds_read_b128 v[208:211], v146 offset:4096
	ds_read_b128 v[212:215], v146 offset:5120
	ds_read_b128 v[216:219], v146 offset:6144
	ds_read_b128 v[220:223], v146 offset:7168
	global_load_lds_dwordx4 v[184:185], off
	v_lshl_add_u64 v[184:185], s[10:11], 0, v[140:141]
	s_add_i32 m0, s24, 0xe000
	s_nop 0
	global_load_lds_dwordx4 v[184:185], off
	s_waitcnt lgkmcnt(8)
	s_setprio 1
	s_barrier
	s_waitcnt lgkmcnt(0)
	v_mfma_f32_16x16x32_bf16 v[124:127], v[148:151], v[164:167], v[124:127]
	v_mfma_f32_16x16x32_bf16 v[104:107], v[156:159], v[164:167], v[104:107]
	v_mfma_f32_16x16x32_bf16 v[120:123], v[148:151], v[176:179], v[120:123]
	v_mfma_f32_16x16x32_bf16 v[92:95], v[156:159], v[176:179], v[92:95]
	v_mfma_f32_16x16x32_bf16 v[116:119], v[148:151], v[208:211], v[116:119]
	v_mfma_f32_16x16x32_bf16 v[84:87], v[156:159], v[208:211], v[84:87]
	v_mfma_f32_16x16x32_bf16 v[112:115], v[148:151], v[216:219], v[112:115]
	v_mfma_f32_16x16x32_bf16 v[80:83], v[156:159], v[216:219], v[80:83]
	v_mfma_f32_16x16x32_bf16 v[124:127], v[152:155], v[172:175], v[124:127]
	v_mfma_f32_16x16x32_bf16 v[104:107], v[160:163], v[172:175], v[104:107]
	v_mfma_f32_16x16x32_bf16 v[120:123], v[152:155], v[180:183], v[120:123]
	v_mfma_f32_16x16x32_bf16 v[92:95], v[160:163], v[180:183], v[92:95]
	v_mfma_f32_16x16x32_bf16 v[116:119], v[152:155], v[212:215], v[116:119]
	v_mfma_f32_16x16x32_bf16 v[84:87], v[160:163], v[212:215], v[84:87]
	v_mfma_f32_16x16x32_bf16 v[112:115], v[152:155], v[220:223], v[112:115]
	v_mfma_f32_16x16x32_bf16 v[80:83], v[160:163], v[220:223], v[80:83]
	s_barrier
	s_setprio 0
	s_add_i32 s39, 0, 0x14000
	s_add_i32 s10, s38, s23
	v_add_u32_e32 v147, s39, v145
	v_lshl_add_u64 v[184:185], s[14:15], 0, v[168:169]
	s_mov_b32 m0, s10
	ds_read_b128 v[224:227], v147
	ds_read_b128 v[228:231], v147 offset:1024
	ds_read_b128 v[232:235], v147 offset:2048
	ds_read_b128 v[236:239], v147 offset:3072
	global_load_lds_dwordx4 v[184:185], off
	v_lshl_add_u64 v[240:241], s[14:15], 0, v[132:133]
	s_add_i32 m0, s10, 0x2000
	s_nop 0
	global_load_lds_dwordx4 v[240:241], off
	s_setprio 1
	s_barrier
	s_waitcnt lgkmcnt(0)
	v_mfma_f32_16x16x32_bf16 v[76:79], v[224:227], v[164:167], v[76:79]
	s_mov_b32 m0, s24
	v_mfma_f32_16x16x32_bf16 v[64:67], v[232:235], v[164:167], v[64:67]
	v_lshl_add_u64 v[242:243], s[16:17], 0, v[134:135]
	v_mfma_f32_16x16x32_bf16 v[68:71], v[224:227], v[176:179], v[68:71]
	v_mfma_f32_16x16x32_bf16 v[52:55], v[232:235], v[176:179], v[52:55]
	v_mfma_f32_16x16x32_bf16 v[56:59], v[224:227], v[208:211], v[56:59]
	v_mfma_f32_16x16x32_bf16 v[44:47], v[232:235], v[208:211], v[44:47]
	v_mfma_f32_16x16x32_bf16 v[48:51], v[224:227], v[216:219], v[48:51]
	v_mfma_f32_16x16x32_bf16 v[32:35], v[232:235], v[216:219], v[32:35]
	v_mfma_f32_16x16x32_bf16 v[76:79], v[228:231], v[172:175], v[76:79]
	v_mfma_f32_16x16x32_bf16 v[64:67], v[236:239], v[172:175], v[64:67]
	v_mfma_f32_16x16x32_bf16 v[68:71], v[228:231], v[180:183], v[68:71]
	v_mfma_f32_16x16x32_bf16 v[52:55], v[236:239], v[180:183], v[52:55]
	v_mfma_f32_16x16x32_bf16 v[56:59], v[228:231], v[212:215], v[56:59]
	v_mfma_f32_16x16x32_bf16 v[44:47], v[236:239], v[212:215], v[44:47]
	v_mfma_f32_16x16x32_bf16 v[48:51], v[228:231], v[220:223], v[48:51]
	v_mfma_f32_16x16x32_bf16 v[32:35], v[236:239], v[220:223], v[32:35]
	s_barrier
	s_setprio 0
	ds_read_b128 v[164:167], v146 offset:16384
	ds_read_b128 v[172:175], v146 offset:17408
	ds_read_b128 v[176:179], v146 offset:18432
	ds_read_b128 v[180:183], v146 offset:19456
	ds_read_b128 v[208:211], v146 offset:20480
	ds_read_b128 v[212:215], v146 offset:21504
	ds_read_b128 v[216:219], v146 offset:22528
	ds_read_b128 v[220:223], v146 offset:23552
	global_load_lds_dwordx4 v[242:243], off
	v_lshl_add_u64 v[244:245], s[16:17], 0, v[128:129]
	s_mov_b32 m0, s25
	s_nop 0
	global_load_lds_dwordx4 v[244:245], off
	s_setprio 1
	s_barrier
	s_waitcnt lgkmcnt(0)
	v_mfma_f32_16x16x32_bf16 v[72:75], v[148:151], v[164:167], v[72:75]
	v_mfma_f32_16x16x32_bf16 v[40:43], v[156:159], v[164:167], v[40:43]
	v_mfma_f32_16x16x32_bf16 v[60:63], v[148:151], v[176:179], v[60:63]
	v_mfma_f32_16x16x32_bf16 v[28:31], v[156:159], v[176:179], v[28:31]
	v_mfma_f32_16x16x32_bf16 v[36:39], v[148:151], v[208:211], v[36:39]
	v_mfma_f32_16x16x32_bf16 v[20:23], v[156:159], v[208:211], v[20:23]
	v_mfma_f32_16x16x32_bf16 v[24:27], v[148:151], v[216:219], v[24:27]
	v_mfma_f32_16x16x32_bf16 v[16:19], v[156:159], v[216:219], v[16:19]
	v_mfma_f32_16x16x32_bf16 v[72:75], v[152:155], v[172:175], v[72:75]
	v_mfma_f32_16x16x32_bf16 v[40:43], v[160:163], v[172:175], v[40:43]
	v_mfma_f32_16x16x32_bf16 v[60:63], v[152:155], v[180:183], v[60:63]
	v_mfma_f32_16x16x32_bf16 v[28:31], v[160:163], v[180:183], v[28:31]
	v_mfma_f32_16x16x32_bf16 v[36:39], v[152:155], v[212:215], v[36:39]
	v_mfma_f32_16x16x32_bf16 v[20:23], v[160:163], v[212:215], v[20:23]
	v_mfma_f32_16x16x32_bf16 v[24:27], v[152:155], v[220:223], v[24:27]
	v_mfma_f32_16x16x32_bf16 v[16:19], v[160:163], v[220:223], v[16:19]
	s_barrier
	s_setprio 0
	s_add_u32 s10, s14, 0x100000
	s_addc_u32 s11, s15, 0
	s_add_i32 s38, s39, s23
	v_lshl_add_u64 v[148:149], s[10:11], 0, v[168:169]
	s_mov_b32 m0, s38
	s_nop 0
	global_load_lds_dwordx4 v[148:149], off
	v_lshl_add_u64 v[148:149], s[10:11], 0, v[132:133]
	s_add_i32 m0, s38, 0x2000
	s_nop 0
	global_load_lds_dwordx4 v[148:149], off
	s_waitcnt vmcnt(6)
	s_setprio 1
	s_barrier
	v_mfma_f32_16x16x32_bf16 v[12:15], v[224:227], v[164:167], v[12:15]
	s_add_i32 s10, 0, 0x18000
	v_mfma_f32_16x16x32_bf16 v[4:7], v[232:235], v[164:167], v[4:7]
	v_add_u32_e32 v147, s10, v145
	v_mfma_f32_16x16x32_bf16 v[8:11], v[224:227], v[176:179], v[8:11]
	v_mfma_f32_16x16x32_bf16 v[0:3], v[232:235], v[176:179], v[0:3]
	v_mfma_f32_16x16x32_bf16 v[96:99], v[224:227], v[208:211], v[96:99]
	v_mfma_f32_16x16x32_bf16 v[88:91], v[232:235], v[208:211], v[88:91]
	v_mfma_f32_16x16x32_bf16 v[108:111], v[224:227], v[216:219], v[108:111]
	v_mfma_f32_16x16x32_bf16 v[100:103], v[232:235], v[216:219], v[100:103]
	v_mfma_f32_16x16x32_bf16 v[12:15], v[228:231], v[172:175], v[12:15]
	v_mfma_f32_16x16x32_bf16 v[4:7], v[236:239], v[172:175], v[4:7]
	v_mfma_f32_16x16x32_bf16 v[8:11], v[228:231], v[180:183], v[8:11]
	v_mfma_f32_16x16x32_bf16 v[0:3], v[236:239], v[180:183], v[0:3]
	v_mfma_f32_16x16x32_bf16 v[96:99], v[228:231], v[212:215], v[96:99]
	v_mfma_f32_16x16x32_bf16 v[88:91], v[236:239], v[212:215], v[88:91]
	v_mfma_f32_16x16x32_bf16 v[108:111], v[228:231], v[220:223], v[108:111]
	v_mfma_f32_16x16x32_bf16 v[100:103], v[236:239], v[220:223], v[100:103]
	s_barrier
	s_setprio 0
	ds_read_b128 v[148:151], v147
	ds_read_b128 v[152:155], v147 offset:1024
	ds_read_b128 v[156:159], v147 offset:2048
	ds_read_b128 v[160:163], v147 offset:3072
	s_mov_b32 m0, s26
	v_lshl_add_u64 v[224:225], s[16:17], 0, v[136:137]
	ds_read_b128 v[164:167], v146 offset:32768
	ds_read_b128 v[172:175], v146 offset:33792
	ds_read_b128 v[176:179], v146 offset:34816
	ds_read_b128 v[180:183], v146 offset:35840
	ds_read_b128 v[208:211], v146 offset:36864
	ds_read_b128 v[212:215], v146 offset:37888
	ds_read_b128 v[216:219], v146 offset:38912
	ds_read_b128 v[220:223], v146 offset:39936
	global_load_lds_dwordx4 v[224:225], off
	v_lshl_add_u64 v[224:225], s[16:17], 0, v[130:131]
	s_mov_b32 m0, s27
	s_nop 0
	global_load_lds_dwordx4 v[224:225], off
	s_waitcnt lgkmcnt(8)
	s_setprio 1
	s_barrier
	s_waitcnt lgkmcnt(0)
	v_mfma_f32_16x16x32_bf16 v[124:127], v[148:151], v[164:167], v[124:127]
	v_mfma_f32_16x16x32_bf16 v[104:107], v[156:159], v[164:167], v[104:107]
	v_mfma_f32_16x16x32_bf16 v[120:123], v[148:151], v[176:179], v[120:123]
	v_mfma_f32_16x16x32_bf16 v[92:95], v[156:159], v[176:179], v[92:95]
	v_mfma_f32_16x16x32_bf16 v[116:119], v[148:151], v[208:211], v[116:119]
	v_mfma_f32_16x16x32_bf16 v[84:87], v[156:159], v[208:211], v[84:87]
	v_mfma_f32_16x16x32_bf16 v[112:115], v[148:151], v[216:219], v[112:115]
	v_mfma_f32_16x16x32_bf16 v[80:83], v[156:159], v[216:219], v[80:83]
	v_mfma_f32_16x16x32_bf16 v[124:127], v[152:155], v[172:175], v[124:127]
	v_mfma_f32_16x16x32_bf16 v[104:107], v[160:163], v[172:175], v[104:107]
	v_mfma_f32_16x16x32_bf16 v[120:123], v[152:155], v[180:183], v[120:123]
	v_mfma_f32_16x16x32_bf16 v[92:95], v[160:163], v[180:183], v[92:95]
	v_mfma_f32_16x16x32_bf16 v[116:119], v[152:155], v[212:215], v[116:119]
	v_mfma_f32_16x16x32_bf16 v[84:87], v[160:163], v[212:215], v[84:87]
	v_mfma_f32_16x16x32_bf16 v[112:115], v[152:155], v[220:223], v[112:115]
	v_mfma_f32_16x16x32_bf16 v[80:83], v[160:163], v[220:223], v[80:83]
	s_barrier
	s_setprio 0
	s_add_i32 s16, 0, 0x1c000
	s_add_i32 s10, s10, s23
	v_add_u32_e32 v147, s16, v145
	v_lshl_add_u64 v[184:185], v[184:185], 0, s[94:95]
	s_mov_b32 m0, s10
	ds_read_b128 v[224:227], v147
	ds_read_b128 v[228:231], v147 offset:1024
	ds_read_b128 v[232:235], v147 offset:2048
	ds_read_b128 v[236:239], v147 offset:3072
	global_load_lds_dwordx4 v[184:185], off
	v_lshl_add_u64 v[184:185], v[240:241], 0, s[94:95]
	s_add_i32 m0, s10, 0x2000
	s_nop 0
	global_load_lds_dwordx4 v[184:185], off
	s_setprio 1
	s_barrier
	s_waitcnt lgkmcnt(0)
	v_mfma_f32_16x16x32_bf16 v[76:79], v[224:227], v[164:167], v[76:79]
	s_mov_b32 m0, s28
	v_mfma_f32_16x16x32_bf16 v[64:67], v[232:235], v[164:167], v[64:67]
	v_lshl_add_u64 v[184:185], v[242:243], 0, s[94:95]
	v_mfma_f32_16x16x32_bf16 v[68:71], v[224:227], v[176:179], v[68:71]
	v_mfma_f32_16x16x32_bf16 v[52:55], v[232:235], v[176:179], v[52:55]
	v_mfma_f32_16x16x32_bf16 v[56:59], v[224:227], v[208:211], v[56:59]
	v_mfma_f32_16x16x32_bf16 v[44:47], v[232:235], v[208:211], v[44:47]
	v_mfma_f32_16x16x32_bf16 v[48:51], v[224:227], v[216:219], v[48:51]
	v_mfma_f32_16x16x32_bf16 v[32:35], v[232:235], v[216:219], v[32:35]
	v_mfma_f32_16x16x32_bf16 v[76:79], v[228:231], v[172:175], v[76:79]
	v_mfma_f32_16x16x32_bf16 v[64:67], v[236:239], v[172:175], v[64:67]
	v_mfma_f32_16x16x32_bf16 v[68:71], v[228:231], v[180:183], v[68:71]
	v_mfma_f32_16x16x32_bf16 v[52:55], v[236:239], v[180:183], v[52:55]
	v_mfma_f32_16x16x32_bf16 v[56:59], v[228:231], v[212:215], v[56:59]
	v_mfma_f32_16x16x32_bf16 v[44:47], v[236:239], v[212:215], v[44:47]
	v_mfma_f32_16x16x32_bf16 v[48:51], v[228:231], v[220:223], v[48:51]
	v_mfma_f32_16x16x32_bf16 v[32:35], v[236:239], v[220:223], v[32:35]
	s_barrier
	s_setprio 0
	ds_read_b128 v[164:167], v146 offset:49152
	ds_read_b128 v[172:175], v146 offset:50176
	ds_read_b128 v[176:179], v146 offset:51200
	ds_read_b128 v[180:183], v146 offset:52224
	ds_read_b128 v[208:211], v146 offset:53248
	ds_read_b128 v[212:215], v146 offset:54272
	ds_read_b128 v[216:219], v146 offset:55296
	ds_read_b128 v[220:223], v146 offset:56320
	global_load_lds_dwordx4 v[184:185], off
	v_lshl_add_u64 v[184:185], v[244:245], 0, s[94:95]
	s_mov_b32 m0, s29
	s_nop 0
	global_load_lds_dwordx4 v[184:185], off
	s_setprio 1
	s_barrier
	s_waitcnt lgkmcnt(0)
	v_mfma_f32_16x16x32_bf16 v[72:75], v[148:151], v[164:167], v[72:75]
	v_mfma_f32_16x16x32_bf16 v[40:43], v[156:159], v[164:167], v[40:43]
	v_mfma_f32_16x16x32_bf16 v[60:63], v[148:151], v[176:179], v[60:63]
	v_mfma_f32_16x16x32_bf16 v[28:31], v[156:159], v[176:179], v[28:31]
	v_mfma_f32_16x16x32_bf16 v[36:39], v[148:151], v[208:211], v[36:39]
	v_mfma_f32_16x16x32_bf16 v[20:23], v[156:159], v[208:211], v[20:23]
	v_mfma_f32_16x16x32_bf16 v[24:27], v[148:151], v[216:219], v[24:27]
	v_mfma_f32_16x16x32_bf16 v[16:19], v[156:159], v[216:219], v[16:19]
	v_mfma_f32_16x16x32_bf16 v[72:75], v[152:155], v[172:175], v[72:75]
	v_mfma_f32_16x16x32_bf16 v[40:43], v[160:163], v[172:175], v[40:43]
	v_mfma_f32_16x16x32_bf16 v[60:63], v[152:155], v[180:183], v[60:63]
	v_mfma_f32_16x16x32_bf16 v[28:31], v[160:163], v[180:183], v[28:31]
	v_mfma_f32_16x16x32_bf16 v[36:39], v[152:155], v[212:215], v[36:39]
	v_mfma_f32_16x16x32_bf16 v[20:23], v[160:163], v[212:215], v[20:23]
	v_mfma_f32_16x16x32_bf16 v[24:27], v[152:155], v[220:223], v[24:27]
	v_mfma_f32_16x16x32_bf16 v[16:19], v[160:163], v[220:223], v[16:19]
	s_barrier
	s_setprio 0
	s_add_u32 s10, s14, 0x100080
	s_addc_u32 s11, s15, 0
	s_add_i32 s14, s16, s23
	v_lshl_add_u64 v[148:149], s[10:11], 0, v[168:169]
	s_mov_b32 m0, s14
	s_nop 0
	global_load_lds_dwordx4 v[148:149], off
	v_lshl_add_u64 v[148:149], s[10:11], 0, v[132:133]
	s_add_i32 m0, s14, 0x2000
	s_nop 0
	global_load_lds_dwordx4 v[148:149], off
	s_waitcnt vmcnt(6)
	s_setprio 1
	s_barrier
	v_mfma_f32_16x16x32_bf16 v[12:15], v[224:227], v[164:167], v[12:15]
	s_add_i32 s37, s37, 2
	v_mfma_f32_16x16x32_bf16 v[4:7], v[232:235], v[164:167], v[4:7]
	s_add_u32 s35, s35, 0x100
	v_mfma_f32_16x16x32_bf16 v[8:11], v[224:227], v[176:179], v[8:11]
	s_addc_u32 s36, s36, 0
	v_mfma_f32_16x16x32_bf16 v[0:3], v[232:235], v[176:179], v[0:3]
	s_cmp_gt_u32 s37, 13
	v_mfma_f32_16x16x32_bf16 v[96:99], v[224:227], v[208:211], v[96:99]
	s_mov_b64 s[10:11], s[12:13]
	v_mfma_f32_16x16x32_bf16 v[88:91], v[232:235], v[208:211], v[88:91]
	v_mfma_f32_16x16x32_bf16 v[108:111], v[224:227], v[216:219], v[108:111]
	v_mfma_f32_16x16x32_bf16 v[100:103], v[232:235], v[216:219], v[100:103]
	v_mfma_f32_16x16x32_bf16 v[12:15], v[228:231], v[172:175], v[12:15]
	v_mfma_f32_16x16x32_bf16 v[4:7], v[236:239], v[172:175], v[4:7]
	v_mfma_f32_16x16x32_bf16 v[8:11], v[228:231], v[180:183], v[8:11]
	v_mfma_f32_16x16x32_bf16 v[0:3], v[236:239], v[180:183], v[0:3]
	v_mfma_f32_16x16x32_bf16 v[96:99], v[228:231], v[212:215], v[96:99]
	v_mfma_f32_16x16x32_bf16 v[88:91], v[236:239], v[212:215], v[88:91]
	v_mfma_f32_16x16x32_bf16 v[108:111], v[228:231], v[220:223], v[108:111]
	v_mfma_f32_16x16x32_bf16 v[100:103], v[236:239], v[220:223], v[100:103]
	s_barrier
	s_setprio 0
	s_cbranch_scc0 .LBB0_424
	s_and_b64 vcc, exec, s[2:3]
	s_cbranch_vccz .LBB0_427
	s_barrier

.LBB0_1002:
	s_add_u32 s22, s4, 0x80
	s_addc_u32 s23, s5, 0
	s_add_i32 s49, 0, 0x10000
	v_add_u32_e32 v84, s49, v181
	ds_read_b128 v[68:71], v84
	ds_read_b128 v[76:79], v84 offset:1024
	ds_read_b128 v[80:83], v84 offset:2048
	ds_read_b128 v[84:87], v84 offset:3072
	s_cmp_eq_u32 s48, 28
	s_cselect_b32 s25, s19, s23
	s_cselect_b32 s24, s18, s22
	s_cselect_b32 s23, s21, s47
	s_cselect_b32 s22, s20, s46
	v_lshl_add_u64 v[166:167], s[4:5], 0, v[164:165]
	s_add_i32 m0, s34, 0xc000
	s_nop 0
	global_load_lds_dwordx4 v[166:167], off
	v_lshl_add_u64 v[166:167], s[4:5], 0, v[162:163]
	s_add_i32 m0, s34, 0xe000
	s_nop 0
	global_load_lds_dwordx4 v[166:167], off
	s_waitcnt lgkmcnt(0)
	s_setprio 1
	s_barrier
	s_waitcnt lgkmcnt(0)
	v_mfma_f32_16x16x32_bf16 v[140:143], v[68:71], v[144:147], v[140:143]
	v_mfma_f32_16x16x32_bf16 v[136:139], v[80:83], v[144:147], v[136:139]
	v_mfma_f32_16x16x32_bf16 v[124:127], v[68:71], v[172:175], v[124:127]
	v_mfma_f32_16x16x32_bf16 v[120:123], v[80:83], v[172:175], v[120:123]
	v_mfma_f32_16x16x32_bf16 v[108:111], v[68:71], v[208:211], v[108:111]
	v_mfma_f32_16x16x32_bf16 v[104:107], v[80:83], v[208:211], v[104:107]
	v_mfma_f32_16x16x32_bf16 v[92:95], v[68:71], v[216:219], v[92:95]
	v_mfma_f32_16x16x32_bf16 v[88:91], v[80:83], v[216:219], v[88:91]
	v_mfma_f32_16x16x32_bf16 v[140:143], v[76:79], v[148:151], v[140:143]
	v_mfma_f32_16x16x32_bf16 v[136:139], v[84:87], v[148:151], v[136:139]
	v_mfma_f32_16x16x32_bf16 v[124:127], v[76:79], v[176:179], v[124:127]
	v_mfma_f32_16x16x32_bf16 v[120:123], v[84:87], v[176:179], v[120:123]
	v_mfma_f32_16x16x32_bf16 v[108:111], v[76:79], v[212:215], v[108:111]
	v_mfma_f32_16x16x32_bf16 v[104:107], v[84:87], v[212:215], v[104:107]
	v_mfma_f32_16x16x32_bf16 v[92:95], v[76:79], v[220:223], v[92:95]
	v_mfma_f32_16x16x32_bf16 v[88:91], v[84:87], v[220:223], v[88:91]
	s_barrier
	s_setprio 0
	s_add_i32 s52, 0, 0x14000
	v_add_u32_e32 v166, s52, v181
	s_add_i32 s49, s49, s31
	ds_read_b128 v[224:227], v166
	ds_read_b128 v[228:231], v166 offset:1024
	ds_read_b128 v[232:235], v166 offset:2048
	ds_read_b128 v[236:239], v166 offset:3072
	v_lshl_add_u64 v[166:167], s[22:23], 0, v[168:169]
	s_mov_b32 m0, s49
	v_lshl_add_u64 v[184:185], s[22:23], 0, v[156:157]
	global_load_lds_dwordx4 v[166:167], off
	s_add_i32 m0, s49, 0x2000
	s_nop 0
	global_load_lds_dwordx4 v[184:185], off
	s_setprio 1
	s_barrier
	s_waitcnt lgkmcnt(0)
	v_mfma_f32_16x16x32_bf16 v[132:135], v[224:227], v[144:147], v[132:135]
	s_mov_b32 m0, s34
	v_mfma_f32_16x16x32_bf16 v[128:131], v[232:235], v[144:147], v[128:131]
	v_lshl_add_u64 v[240:241], s[24:25], 0, v[152:153]
	ds_read_b128 v[144:147], v183 offset:16384
	v_mfma_f32_16x16x32_bf16 v[116:119], v[224:227], v[172:175], v[116:119]
	v_mfma_f32_16x16x32_bf16 v[112:115], v[232:235], v[172:175], v[112:115]
	ds_read_b128 v[172:175], v183 offset:18432
	v_mfma_f32_16x16x32_bf16 v[100:103], v[224:227], v[208:211], v[100:103]
	v_mfma_f32_16x16x32_bf16 v[96:99], v[232:235], v[208:211], v[96:99]
	ds_read_b128 v[208:211], v183 offset:20480
	v_mfma_f32_16x16x32_bf16 v[72:75], v[224:227], v[216:219], v[72:75]
	v_mfma_f32_16x16x32_bf16 v[64:67], v[232:235], v[216:219], v[64:67]
	ds_read_b128 v[216:219], v183 offset:22528
	v_mfma_f32_16x16x32_bf16 v[132:135], v[228:231], v[148:151], v[132:135]
	v_mfma_f32_16x16x32_bf16 v[128:131], v[236:239], v[148:151], v[128:131]
	ds_read_b128 v[148:151], v183 offset:17408
	v_mfma_f32_16x16x32_bf16 v[116:119], v[228:231], v[176:179], v[116:119]
	v_mfma_f32_16x16x32_bf16 v[112:115], v[236:239], v[176:179], v[112:115]
	ds_read_b128 v[176:179], v183 offset:19456
	v_mfma_f32_16x16x32_bf16 v[100:103], v[228:231], v[212:215], v[100:103]
	v_mfma_f32_16x16x32_bf16 v[96:99], v[236:239], v[212:215], v[96:99]
	ds_read_b128 v[212:215], v183 offset:21504
	v_mfma_f32_16x16x32_bf16 v[72:75], v[228:231], v[220:223], v[72:75]
	v_mfma_f32_16x16x32_bf16 v[64:67], v[236:239], v[220:223], v[64:67]
	ds_read_b128 v[220:223], v183 offset:23552
	s_barrier
	s_setprio 0
	global_load_lds_dwordx4 v[240:241], off
	v_lshl_add_u64 v[242:243], s[24:25], 0, v[158:159]
	s_mov_b32 m0, s35
	s_nop 0
	global_load_lds_dwordx4 v[242:243], off
	s_waitcnt vmcnt(8)
	s_setprio 1
	s_barrier
	s_waitcnt lgkmcnt(0)
	v_mfma_f32_16x16x32_bf16 v[60:63], v[68:71], v[144:147], v[60:63]
	v_mfma_f32_16x16x32_bf16 v[56:59], v[80:83], v[144:147], v[56:59]
	v_mfma_f32_16x16x32_bf16 v[44:47], v[68:71], v[172:175], v[44:47]
	v_mfma_f32_16x16x32_bf16 v[40:43], v[80:83], v[172:175], v[40:43]
	v_mfma_f32_16x16x32_bf16 v[28:31], v[68:71], v[208:211], v[28:31]
	v_mfma_f32_16x16x32_bf16 v[20:23], v[80:83], v[208:211], v[20:23]
	v_mfma_f32_16x16x32_bf16 v[8:11], v[68:71], v[216:219], v[8:11]
	v_mfma_f32_16x16x32_bf16 v[0:3], v[80:83], v[216:219], v[0:3]
	v_mfma_f32_16x16x32_bf16 v[60:63], v[76:79], v[148:151], v[60:63]
	v_mfma_f32_16x16x32_bf16 v[56:59], v[84:87], v[148:151], v[56:59]
	v_mfma_f32_16x16x32_bf16 v[44:47], v[76:79], v[176:179], v[44:47]
	v_mfma_f32_16x16x32_bf16 v[40:43], v[84:87], v[176:179], v[40:43]
	v_mfma_f32_16x16x32_bf16 v[28:31], v[76:79], v[212:215], v[28:31]
	v_mfma_f32_16x16x32_bf16 v[20:23], v[84:87], v[212:215], v[20:23]
	v_mfma_f32_16x16x32_bf16 v[8:11], v[76:79], v[220:223], v[8:11]
	v_mfma_f32_16x16x32_bf16 v[0:3], v[84:87], v[220:223], v[0:3]
	s_barrier
	s_setprio 0
	s_add_u32 s50, s22, 0x80000
	s_addc_u32 s51, s23, 0
	s_add_i32 s49, s52, s31
	v_lshl_add_u64 v[68:69], s[50:51], 0, v[168:169]
	s_mov_b32 m0, s49
	s_nop 0
	global_load_lds_dwordx4 v[68:69], off
	v_lshl_add_u64 v[68:69], s[50:51], 0, v[156:157]
	s_add_i32 m0, s49, 0x2000
	s_nop 0
	global_load_lds_dwordx4 v[68:69], off
	s_waitcnt vmcnt(6)
	s_setprio 1
	s_barrier
	v_mfma_f32_16x16x32_bf16 v[52:55], v[224:227], v[144:147], v[52:55]
	s_add_i32 s49, 0, 0x18000
	v_mfma_f32_16x16x32_bf16 v[48:51], v[232:235], v[144:147], v[48:51]
	v_add_u32_e32 v84, s49, v181
	ds_read_b128 v[144:147], v183 offset:32768
	v_mfma_f32_16x16x32_bf16 v[36:39], v[224:227], v[172:175], v[36:39]
	v_mfma_f32_16x16x32_bf16 v[32:35], v[232:235], v[172:175], v[32:35]
	ds_read_b128 v[172:175], v183 offset:34816
	v_mfma_f32_16x16x32_bf16 v[24:27], v[224:227], v[208:211], v[24:27]
	v_mfma_f32_16x16x32_bf16 v[16:19], v[232:235], v[208:211], v[16:19]
	ds_read_b128 v[208:211], v183 offset:36864
	v_mfma_f32_16x16x32_bf16 v[12:15], v[224:227], v[216:219], v[12:15]
	v_mfma_f32_16x16x32_bf16 v[4:7], v[232:235], v[216:219], v[4:7]
	ds_read_b128 v[216:219], v183 offset:38912
	v_mfma_f32_16x16x32_bf16 v[52:55], v[228:231], v[148:151], v[52:55]
	v_mfma_f32_16x16x32_bf16 v[48:51], v[236:239], v[148:151], v[48:51]
	ds_read_b128 v[148:151], v183 offset:33792
	v_mfma_f32_16x16x32_bf16 v[36:39], v[228:231], v[176:179], v[36:39]
	v_mfma_f32_16x16x32_bf16 v[32:35], v[236:239], v[176:179], v[32:35]
	ds_read_b128 v[176:179], v183 offset:35840
	v_mfma_f32_16x16x32_bf16 v[24:27], v[228:231], v[212:215], v[24:27]
	v_mfma_f32_16x16x32_bf16 v[16:19], v[236:239], v[212:215], v[16:19]
	ds_read_b128 v[212:215], v183 offset:37888
	v_mfma_f32_16x16x32_bf16 v[12:15], v[228:231], v[220:223], v[12:15]
	v_mfma_f32_16x16x32_bf16 v[4:7], v[236:239], v[220:223], v[4:7]
	ds_read_b128 v[220:223], v183 offset:39936
	s_barrier
	s_setprio 0
	ds_read_b128 v[68:71], v84
	ds_read_b128 v[76:79], v84 offset:1024
	ds_read_b128 v[80:83], v84 offset:2048
	ds_read_b128 v[84:87], v84 offset:3072
	s_mov_b32 m0, s36
	v_lshl_add_u64 v[224:225], s[24:25], 0, v[154:155]
	global_load_lds_dwordx4 v[224:225], off
	v_lshl_add_u64 v[224:225], s[24:25], 0, v[160:161]
	s_mov_b32 m0, s37
	s_nop 0
	global_load_lds_dwordx4 v[224:225], off
	s_waitcnt lgkmcnt(0)
	s_setprio 1
	s_barrier
	s_waitcnt lgkmcnt(0)
	v_mfma_f32_16x16x32_bf16 v[140:143], v[68:71], v[144:147], v[140:143]
	v_mfma_f32_16x16x32_bf16 v[136:139], v[80:83], v[144:147], v[136:139]
	v_mfma_f32_16x16x32_bf16 v[124:127], v[68:71], v[172:175], v[124:127]
	v_mfma_f32_16x16x32_bf16 v[120:123], v[80:83], v[172:175], v[120:123]
	v_mfma_f32_16x16x32_bf16 v[108:111], v[68:71], v[208:211], v[108:111]
	v_mfma_f32_16x16x32_bf16 v[104:107], v[80:83], v[208:211], v[104:107]
	v_mfma_f32_16x16x32_bf16 v[92:95], v[68:71], v[216:219], v[92:95]
	v_mfma_f32_16x16x32_bf16 v[88:91], v[80:83], v[216:219], v[88:91]
	v_mfma_f32_16x16x32_bf16 v[140:143], v[76:79], v[148:151], v[140:143]
	v_mfma_f32_16x16x32_bf16 v[136:139], v[84:87], v[148:151], v[136:139]
	v_mfma_f32_16x16x32_bf16 v[124:127], v[76:79], v[176:179], v[124:127]
	v_mfma_f32_16x16x32_bf16 v[120:123], v[84:87], v[176:179], v[120:123]
	v_mfma_f32_16x16x32_bf16 v[108:111], v[76:79], v[212:215], v[108:111]
	v_mfma_f32_16x16x32_bf16 v[104:107], v[84:87], v[212:215], v[104:107]
	v_mfma_f32_16x16x32_bf16 v[92:95], v[76:79], v[220:223], v[92:95]
	v_mfma_f32_16x16x32_bf16 v[88:91], v[84:87], v[220:223], v[88:91]
	s_barrier
	s_setprio 0
	s_add_i32 s24, 0, 0x1c000
	s_add_i32 s25, s49, s31
	v_add_u32_e32 v170, s24, v181
	v_lshl_add_u64 v[166:167], v[166:167], 0, s[94:95]
	s_mov_b32 m0, s25
	ds_read_b128 v[224:227], v170
	ds_read_b128 v[228:231], v170 offset:1024
	ds_read_b128 v[232:235], v170 offset:2048
	ds_read_b128 v[236:239], v170 offset:3072
	global_load_lds_dwordx4 v[166:167], off
	v_lshl_add_u64 v[166:167], v[184:185], 0, s[94:95]
	s_add_i32 m0, s25, 0x2000
	s_nop 0
	global_load_lds_dwordx4 v[166:167], off
	s_setprio 1
	s_barrier
	s_waitcnt lgkmcnt(0)
	v_mfma_f32_16x16x32_bf16 v[132:135], v[224:227], v[144:147], v[132:135]
	s_mov_b32 m0, s40
	v_mfma_f32_16x16x32_bf16 v[128:131], v[232:235], v[144:147], v[128:131]
	v_lshl_add_u64 v[166:167], v[240:241], 0, s[94:95]
	ds_read_b128 v[144:147], v183 offset:49152
	v_mfma_f32_16x16x32_bf16 v[116:119], v[224:227], v[172:175], v[116:119]
	v_mfma_f32_16x16x32_bf16 v[112:115], v[232:235], v[172:175], v[112:115]
	ds_read_b128 v[172:175], v183 offset:51200
	v_mfma_f32_16x16x32_bf16 v[100:103], v[224:227], v[208:211], v[100:103]
	v_mfma_f32_16x16x32_bf16 v[96:99], v[232:235], v[208:211], v[96:99]
	ds_read_b128 v[208:211], v183 offset:53248
	v_mfma_f32_16x16x32_bf16 v[72:75], v[224:227], v[216:219], v[72:75]
	v_mfma_f32_16x16x32_bf16 v[64:67], v[232:235], v[216:219], v[64:67]
	ds_read_b128 v[216:219], v183 offset:55296
	v_mfma_f32_16x16x32_bf16 v[132:135], v[228:231], v[148:151], v[132:135]
	v_mfma_f32_16x16x32_bf16 v[128:131], v[236:239], v[148:151], v[128:131]
	ds_read_b128 v[148:151], v183 offset:50176
	v_mfma_f32_16x16x32_bf16 v[116:119], v[228:231], v[176:179], v[116:119]
	v_mfma_f32_16x16x32_bf16 v[112:115], v[236:239], v[176:179], v[112:115]
	ds_read_b128 v[176:179], v183 offset:52224
	v_mfma_f32_16x16x32_bf16 v[100:103], v[228:231], v[212:215], v[100:103]
	v_mfma_f32_16x16x32_bf16 v[96:99], v[236:239], v[212:215], v[96:99]
	ds_read_b128 v[212:215], v183 offset:54272
	v_mfma_f32_16x16x32_bf16 v[72:75], v[228:231], v[220:223], v[72:75]
	v_mfma_f32_16x16x32_bf16 v[64:67], v[236:239], v[220:223], v[64:67]
	ds_read_b128 v[220:223], v183 offset:56320
	s_barrier
	s_setprio 0
	global_load_lds_dwordx4 v[166:167], off
	v_lshl_add_u64 v[166:167], v[242:243], 0, s[94:95]
	s_mov_b32 m0, s41
	s_nop 0
	global_load_lds_dwordx4 v[166:167], off
	s_waitcnt vmcnt(8)
	s_setprio 1
	s_barrier
	s_waitcnt lgkmcnt(0)
	v_mfma_f32_16x16x32_bf16 v[60:63], v[68:71], v[144:147], v[60:63]
	v_mfma_f32_16x16x32_bf16 v[56:59], v[80:83], v[144:147], v[56:59]
	v_mfma_f32_16x16x32_bf16 v[44:47], v[68:71], v[172:175], v[44:47]
	v_mfma_f32_16x16x32_bf16 v[40:43], v[80:83], v[172:175], v[40:43]
	v_mfma_f32_16x16x32_bf16 v[28:31], v[68:71], v[208:211], v[28:31]
	v_mfma_f32_16x16x32_bf16 v[20:23], v[80:83], v[208:211], v[20:23]
	v_mfma_f32_16x16x32_bf16 v[8:11], v[68:71], v[216:219], v[8:11]
	v_mfma_f32_16x16x32_bf16 v[0:3], v[80:83], v[216:219], v[0:3]
	v_mfma_f32_16x16x32_bf16 v[60:63], v[76:79], v[148:151], v[60:63]
	v_mfma_f32_16x16x32_bf16 v[56:59], v[84:87], v[148:151], v[56:59]
	v_mfma_f32_16x16x32_bf16 v[44:47], v[76:79], v[176:179], v[44:47]
	v_mfma_f32_16x16x32_bf16 v[40:43], v[84:87], v[176:179], v[40:43]
	v_mfma_f32_16x16x32_bf16 v[28:31], v[76:79], v[212:215], v[28:31]
	v_mfma_f32_16x16x32_bf16 v[20:23], v[84:87], v[212:215], v[20:23]
	v_mfma_f32_16x16x32_bf16 v[8:11], v[76:79], v[220:223], v[8:11]
	v_mfma_f32_16x16x32_bf16 v[0:3], v[84:87], v[220:223], v[0:3]
	s_barrier
	s_setprio 0
	s_add_u32 s22, s22, 0x80080
	s_addc_u32 s23, s23, 0
	s_add_i32 s24, s24, s31
	v_lshl_add_u64 v[68:69], s[22:23], 0, v[168:169]
	s_mov_b32 m0, s24
	s_nop 0
	global_load_lds_dwordx4 v[68:69], off
	v_lshl_add_u64 v[68:69], s[22:23], 0, v[156:157]
	s_add_i32 m0, s24, 0x2000
	s_nop 0
	global_load_lds_dwordx4 v[68:69], off
	s_waitcnt vmcnt(6)
	s_setprio 1
	s_barrier
	v_mfma_f32_16x16x32_bf16 v[52:55], v[224:227], v[144:147], v[52:55]
	s_add_i32 s48, s48, 2
	v_mfma_f32_16x16x32_bf16 v[48:51], v[232:235], v[144:147], v[48:51]
	s_add_u32 s4, s4, 0x100
	ds_read_b128 v[144:147], v183
	v_mfma_f32_16x16x32_bf16 v[36:39], v[224:227], v[172:175], v[36:39]
	s_addc_u32 s5, s5, 0
	v_mfma_f32_16x16x32_bf16 v[32:35], v[232:235], v[172:175], v[32:35]
	s_add_u32 s46, s46, 0x100
	ds_read_b128 v[172:175], v183 offset:2048
	v_mfma_f32_16x16x32_bf16 v[24:27], v[224:227], v[208:211], v[24:27]
	s_addc_u32 s47, s47, 0
	v_mfma_f32_16x16x32_bf16 v[16:19], v[232:235], v[208:211], v[16:19]
	s_cmp_gt_u32 s48, 29
	ds_read_b128 v[208:211], v183 offset:4096
	v_mfma_f32_16x16x32_bf16 v[12:15], v[224:227], v[216:219], v[12:15]
	v_mfma_f32_16x16x32_bf16 v[4:7], v[232:235], v[216:219], v[4:7]
	ds_read_b128 v[216:219], v183 offset:6144
	v_mfma_f32_16x16x32_bf16 v[52:55], v[228:231], v[148:151], v[52:55]
	v_mfma_f32_16x16x32_bf16 v[48:51], v[236:239], v[148:151], v[48:51]
	ds_read_b128 v[148:151], v183 offset:1024
	v_mfma_f32_16x16x32_bf16 v[36:39], v[228:231], v[176:179], v[36:39]
	v_mfma_f32_16x16x32_bf16 v[32:35], v[236:239], v[176:179], v[32:35]
	ds_read_b128 v[176:179], v183 offset:3072
	v_mfma_f32_16x16x32_bf16 v[24:27], v[228:231], v[212:215], v[24:27]
	v_mfma_f32_16x16x32_bf16 v[16:19], v[236:239], v[212:215], v[16:19]
	ds_read_b128 v[212:215], v183 offset:5120
	v_mfma_f32_16x16x32_bf16 v[12:15], v[228:231], v[220:223], v[12:15]
	v_mfma_f32_16x16x32_bf16 v[4:7], v[236:239], v[220:223], v[4:7]
	ds_read_b128 v[220:223], v183 offset:7168
	s_barrier
	s_setprio 0
	s_cbranch_scc0 .LBB0_1002
	s_waitcnt lgkmcnt(0)
	s_and_b64 vcc, exec, s[14:15]
	s_cbranch_vccz .LBB0_1005
	s_barrier

.LBB0_1423:
	s_add_u32 s36, s26, s34
	s_addc_u32 s37, s27, s35
	s_add_u32 s38, s36, 0x100
	s_addc_u32 s39, s37, 0
	s_add_u32 s58, s23, s34
	s_addc_u32 s59, s56, s35
	s_add_i32 s60, 0, 0x10000
	v_add_u32_e32 v141, s60, v135
	ds_read_b128 v[158:161], v141
	ds_read_b128 v[162:165], v141 offset:1024
	ds_read_b128 v[172:175], v141 offset:2048
	ds_read_b128 v[176:179], v141 offset:3072
	s_cmpk_eq_i32 s34, 0xf00
	s_cselect_b64 vcc, -1, 0
	s_and_b64 s[36:37], vcc, exec
	v_cndmask_b32_e32 v168, v134, v154, vcc
	v_cndmask_b32_e32 v166, v132, v155, vcc
	v_cndmask_b32_e32 v129, v128, v153, vcc
	v_cndmask_b32_e32 v139, v138, v156, vcc
	s_cselect_b32 s39, s31, s39
	s_cselect_b32 s38, s30, s38
	s_cselect_b32 s37, s5, s59
	s_cselect_b32 s36, s4, s58
	v_lshl_add_u64 v[184:185], v[144:145], 0, s[34:35]
	s_add_i32 m0, s43, 0xc000
	s_nop 0
	global_load_lds_dwordx4 v[184:185], off
	v_lshl_add_u64 v[184:185], v[142:143], 0, s[34:35]
	s_add_i32 m0, s43, 0xe000
	s_nop 0
	global_load_lds_dwordx4 v[184:185], off
	s_waitcnt lgkmcnt(0)
	s_setprio 1
	s_barrier
	s_waitcnt lgkmcnt(0)
	v_mfma_f32_16x16x32_bf16 v[124:127], v[158:161], v[180:183], v[124:127]
	v_mfma_f32_16x16x32_bf16 v[120:123], v[172:175], v[180:183], v[120:123]
	v_mfma_f32_16x16x32_bf16 v[116:119], v[158:161], v[212:215], v[116:119]
	v_mfma_f32_16x16x32_bf16 v[112:115], v[172:175], v[212:215], v[112:115]
	v_mfma_f32_16x16x32_bf16 v[108:111], v[158:161], v[220:223], v[108:111]
	v_mfma_f32_16x16x32_bf16 v[104:107], v[172:175], v[220:223], v[104:107]
	v_mfma_f32_16x16x32_bf16 v[100:103], v[158:161], v[228:231], v[100:103]
	v_mfma_f32_16x16x32_bf16 v[96:99], v[172:175], v[228:231], v[96:99]
	v_mfma_f32_16x16x32_bf16 v[124:127], v[162:165], v[208:211], v[124:127]
	v_mfma_f32_16x16x32_bf16 v[120:123], v[176:179], v[208:211], v[120:123]
	v_mfma_f32_16x16x32_bf16 v[116:119], v[162:165], v[216:219], v[116:119]
	v_mfma_f32_16x16x32_bf16 v[112:115], v[176:179], v[216:219], v[112:115]
	v_mfma_f32_16x16x32_bf16 v[108:111], v[162:165], v[224:227], v[108:111]
	v_mfma_f32_16x16x32_bf16 v[104:107], v[176:179], v[224:227], v[104:107]
	v_mfma_f32_16x16x32_bf16 v[100:103], v[162:165], v[232:235], v[100:103]
	v_mfma_f32_16x16x32_bf16 v[96:99], v[176:179], v[232:235], v[96:99]
	s_barrier
	s_setprio 0
	s_add_i32 s61, 0, 0x14000
	s_add_i32 s58, s60, s9
	v_add_u32_e32 v141, s61, v135
	v_lshl_add_u64 v[184:185], s[36:37], 0, v[130:131]
	s_mov_b32 m0, s58
	ds_read_b128 v[236:239], v141
	ds_read_b128 v[240:243], v141 offset:1024
	ds_read_b128 v[244:247], v141 offset:2048
	ds_read_b128 v[248:251], v141 offset:3072
	global_load_lds_dwordx4 v[184:185], off
	v_lshl_add_u64 v[188:189], s[36:37], 0, v[136:137]
	s_add_i32 m0, s58, 0x2000
	s_nop 0
	global_load_lds_dwordx4 v[188:189], off
	s_setprio 1
	s_barrier
	s_waitcnt lgkmcnt(0)
	v_mfma_f32_16x16x32_bf16 v[92:95], v[236:239], v[180:183], v[92:95]
	s_mov_b32 m0, s43
	v_mfma_f32_16x16x32_bf16 v[88:91], v[244:247], v[180:183], v[88:91]
	ds_read_b128 v[180:183], v152 offset:16384
	v_mfma_f32_16x16x32_bf16 v[84:87], v[236:239], v[212:215], v[84:87]
	v_mfma_f32_16x16x32_bf16 v[80:83], v[244:247], v[212:215], v[80:83]
	ds_read_b128 v[212:215], v152 offset:18432
	v_mfma_f32_16x16x32_bf16 v[76:79], v[236:239], v[220:223], v[76:79]
	v_mfma_f32_16x16x32_bf16 v[72:75], v[244:247], v[220:223], v[72:75]
	ds_read_b128 v[220:223], v152 offset:20480
	v_mfma_f32_16x16x32_bf16 v[68:71], v[236:239], v[228:231], v[68:71]
	v_mfma_f32_16x16x32_bf16 v[64:67], v[244:247], v[228:231], v[64:67]
	ds_read_b128 v[228:231], v152 offset:22528
	v_mfma_f32_16x16x32_bf16 v[92:95], v[240:243], v[208:211], v[92:95]
	v_mfma_f32_16x16x32_bf16 v[88:91], v[248:251], v[208:211], v[88:91]
	ds_read_b128 v[208:211], v152 offset:17408
	v_mfma_f32_16x16x32_bf16 v[84:87], v[240:243], v[216:219], v[84:87]
	v_mfma_f32_16x16x32_bf16 v[80:83], v[248:251], v[216:219], v[80:83]
	ds_read_b128 v[216:219], v152 offset:19456
	v_mfma_f32_16x16x32_bf16 v[76:79], v[240:243], v[224:227], v[76:79]
	v_mfma_f32_16x16x32_bf16 v[72:75], v[248:251], v[224:227], v[72:75]
	ds_read_b128 v[224:227], v152 offset:21504
	v_mfma_f32_16x16x32_bf16 v[68:71], v[240:243], v[232:235], v[68:71]
	v_mfma_f32_16x16x32_bf16 v[64:67], v[248:251], v[232:235], v[64:67]
	ds_read_b128 v[232:235], v152 offset:23552
	s_barrier
	s_setprio 0
	global_load_lds_dwordx4 v168, s[38:39]
	s_mov_b32 m0, s44
	v_mov_b32_e32 v167, v169
	global_load_lds_dwordx4 v166, s[38:39]
	s_waitcnt vmcnt(8)
	v_lshl_add_u64 v[170:171], s[38:39], 0, v[168:169]
	v_lshl_add_u64 v[166:167], s[38:39], 0, v[166:167]
	s_setprio 1
	s_barrier
	s_waitcnt lgkmcnt(0)
	v_mfma_f32_16x16x32_bf16 v[60:63], v[158:161], v[180:183], v[60:63]
	v_mfma_f32_16x16x32_bf16 v[56:59], v[172:175], v[180:183], v[56:59]
	v_mfma_f32_16x16x32_bf16 v[52:55], v[158:161], v[212:215], v[52:55]
	v_mfma_f32_16x16x32_bf16 v[48:51], v[172:175], v[212:215], v[48:51]
	v_mfma_f32_16x16x32_bf16 v[44:47], v[158:161], v[220:223], v[44:47]
	v_mfma_f32_16x16x32_bf16 v[40:43], v[172:175], v[220:223], v[40:43]
	v_mfma_f32_16x16x32_bf16 v[36:39], v[158:161], v[228:231], v[36:39]
	v_mfma_f32_16x16x32_bf16 v[32:35], v[172:175], v[228:231], v[32:35]
	v_mfma_f32_16x16x32_bf16 v[60:63], v[162:165], v[208:211], v[60:63]
	v_mfma_f32_16x16x32_bf16 v[56:59], v[176:179], v[208:211], v[56:59]
	v_mfma_f32_16x16x32_bf16 v[52:55], v[162:165], v[216:219], v[52:55]
	v_mfma_f32_16x16x32_bf16 v[48:51], v[176:179], v[216:219], v[48:51]
	v_mfma_f32_16x16x32_bf16 v[44:47], v[162:165], v[224:227], v[44:47]
	v_mfma_f32_16x16x32_bf16 v[40:43], v[176:179], v[224:227], v[40:43]
	v_mfma_f32_16x16x32_bf16 v[36:39], v[162:165], v[232:235], v[36:39]
	v_mfma_f32_16x16x32_bf16 v[32:35], v[176:179], v[232:235], v[32:35]
	s_barrier
	s_setprio 0
	s_add_u32 s58, s36, 0x80000
	s_addc_u32 s59, s37, 0
	s_add_i32 s60, s61, s9
	v_lshl_add_u64 v[158:159], s[58:59], 0, v[130:131]
	s_mov_b32 m0, s60
	s_nop 0
	global_load_lds_dwordx4 v[158:159], off
	v_lshl_add_u64 v[158:159], s[58:59], 0, v[136:137]
	s_add_i32 m0, s60, 0x2000
	s_nop 0
	global_load_lds_dwordx4 v[158:159], off
	s_waitcnt vmcnt(6)
	s_setprio 1
	s_barrier
	v_mfma_f32_16x16x32_bf16 v[28:31], v[236:239], v[180:183], v[28:31]
	s_add_i32 s58, 0, 0x18000
	v_mfma_f32_16x16x32_bf16 v[24:27], v[244:247], v[180:183], v[24:27]
	v_add_u32_e32 v141, s58, v135
	ds_read_b128 v[180:183], v152 offset:32768
	v_mfma_f32_16x16x32_bf16 v[20:23], v[236:239], v[212:215], v[20:23]
	v_mfma_f32_16x16x32_bf16 v[16:19], v[244:247], v[212:215], v[16:19]
	ds_read_b128 v[212:215], v152 offset:34816
	v_mfma_f32_16x16x32_bf16 v[12:15], v[236:239], v[220:223], v[12:15]
	v_mfma_f32_16x16x32_bf16 v[8:11], v[244:247], v[220:223], v[8:11]
	ds_read_b128 v[220:223], v152 offset:36864
	v_mfma_f32_16x16x32_bf16 v[4:7], v[236:239], v[228:231], v[4:7]
	v_mfma_f32_16x16x32_bf16 v[0:3], v[244:247], v[228:231], v[0:3]
	ds_read_b128 v[228:231], v152 offset:38912
	v_mfma_f32_16x16x32_bf16 v[28:31], v[240:243], v[208:211], v[28:31]
	v_mfma_f32_16x16x32_bf16 v[24:27], v[248:251], v[208:211], v[24:27]
	ds_read_b128 v[208:211], v152 offset:33792
	v_mfma_f32_16x16x32_bf16 v[20:23], v[240:243], v[216:219], v[20:23]
	v_mfma_f32_16x16x32_bf16 v[16:19], v[248:251], v[216:219], v[16:19]
	ds_read_b128 v[216:219], v152 offset:35840
	v_mfma_f32_16x16x32_bf16 v[12:15], v[240:243], v[224:227], v[12:15]
	v_mfma_f32_16x16x32_bf16 v[8:11], v[248:251], v[224:227], v[8:11]
	ds_read_b128 v[224:227], v152 offset:37888
	v_mfma_f32_16x16x32_bf16 v[4:7], v[240:243], v[232:235], v[4:7]
	v_mfma_f32_16x16x32_bf16 v[0:3], v[248:251], v[232:235], v[0:3]
	ds_read_b128 v[232:235], v152 offset:39936
	s_barrier
	s_setprio 0
	ds_read_b128 v[158:161], v141
	ds_read_b128 v[162:165], v141 offset:1024
	ds_read_b128 v[172:175], v141 offset:2048
	ds_read_b128 v[176:179], v141 offset:3072
	s_mov_b32 m0, s45
	s_nop 0
	global_load_lds_dwordx4 v129, s[38:39]
	s_mov_b32 m0, s46
	s_nop 0
	global_load_lds_dwordx4 v139, s[38:39]
	s_waitcnt lgkmcnt(0)
	s_setprio 1
	s_barrier
	s_waitcnt lgkmcnt(0)
	v_mfma_f32_16x16x32_bf16 v[124:127], v[158:161], v[180:183], v[124:127]
	v_mfma_f32_16x16x32_bf16 v[120:123], v[172:175], v[180:183], v[120:123]
	v_mfma_f32_16x16x32_bf16 v[116:119], v[158:161], v[212:215], v[116:119]
	v_mfma_f32_16x16x32_bf16 v[112:115], v[172:175], v[212:215], v[112:115]
	v_mfma_f32_16x16x32_bf16 v[108:111], v[158:161], v[220:223], v[108:111]
	v_mfma_f32_16x16x32_bf16 v[104:107], v[172:175], v[220:223], v[104:107]
	v_mfma_f32_16x16x32_bf16 v[100:103], v[158:161], v[228:231], v[100:103]
	v_mfma_f32_16x16x32_bf16 v[96:99], v[172:175], v[228:231], v[96:99]
	v_mfma_f32_16x16x32_bf16 v[124:127], v[162:165], v[208:211], v[124:127]
	v_mfma_f32_16x16x32_bf16 v[120:123], v[176:179], v[208:211], v[120:123]
	v_mfma_f32_16x16x32_bf16 v[116:119], v[162:165], v[216:219], v[116:119]
	v_mfma_f32_16x16x32_bf16 v[112:115], v[176:179], v[216:219], v[112:115]
	v_mfma_f32_16x16x32_bf16 v[108:111], v[162:165], v[224:227], v[108:111]
	v_mfma_f32_16x16x32_bf16 v[104:107], v[176:179], v[224:227], v[104:107]
	v_mfma_f32_16x16x32_bf16 v[100:103], v[162:165], v[232:235], v[100:103]
	v_mfma_f32_16x16x32_bf16 v[96:99], v[176:179], v[232:235], v[96:99]
	s_barrier
	s_setprio 0
	s_add_i32 s38, 0, 0x1c000
	s_add_i32 s39, s58, s9
	v_add_u32_e32 v129, s38, v135
	v_lshl_add_u64 v[184:185], v[184:185], 0, s[94:95]
	s_mov_b32 m0, s39
	ds_read_b128 v[236:239], v129
	ds_read_b128 v[240:243], v129 offset:1024
	ds_read_b128 v[244:247], v129 offset:2048
	ds_read_b128 v[248:251], v129 offset:3072
	global_load_lds_dwordx4 v[184:185], off
	v_lshl_add_u64 v[184:185], v[188:189], 0, s[94:95]
	s_add_i32 m0, s39, 0x2000
	s_nop 0
	global_load_lds_dwordx4 v[184:185], off
	s_setprio 1
	s_barrier
	s_waitcnt lgkmcnt(0)
	v_mfma_f32_16x16x32_bf16 v[92:95], v[236:239], v[180:183], v[92:95]
	s_mov_b32 m0, s47
	v_mfma_f32_16x16x32_bf16 v[88:91], v[244:247], v[180:183], v[88:91]
	v_lshl_add_u64 v[170:171], v[170:171], 0, s[94:95]
	ds_read_b128 v[180:183], v152 offset:49152
	v_mfma_f32_16x16x32_bf16 v[84:87], v[236:239], v[212:215], v[84:87]
	v_mfma_f32_16x16x32_bf16 v[80:83], v[244:247], v[212:215], v[80:83]
	ds_read_b128 v[212:215], v152 offset:51200
	v_mfma_f32_16x16x32_bf16 v[76:79], v[236:239], v[220:223], v[76:79]
	v_mfma_f32_16x16x32_bf16 v[72:75], v[244:247], v[220:223], v[72:75]
	ds_read_b128 v[220:223], v152 offset:53248
	v_mfma_f32_16x16x32_bf16 v[68:71], v[236:239], v[228:231], v[68:71]
	v_mfma_f32_16x16x32_bf16 v[64:67], v[244:247], v[228:231], v[64:67]
	ds_read_b128 v[228:231], v152 offset:55296
	v_mfma_f32_16x16x32_bf16 v[92:95], v[240:243], v[208:211], v[92:95]
	v_mfma_f32_16x16x32_bf16 v[88:91], v[248:251], v[208:211], v[88:91]
	ds_read_b128 v[208:211], v152 offset:50176
	v_mfma_f32_16x16x32_bf16 v[84:87], v[240:243], v[216:219], v[84:87]
	v_mfma_f32_16x16x32_bf16 v[80:83], v[248:251], v[216:219], v[80:83]
	ds_read_b128 v[216:219], v152 offset:52224
	v_mfma_f32_16x16x32_bf16 v[76:79], v[240:243], v[224:227], v[76:79]
	v_mfma_f32_16x16x32_bf16 v[72:75], v[248:251], v[224:227], v[72:75]
	ds_read_b128 v[224:227], v152 offset:54272
	v_mfma_f32_16x16x32_bf16 v[68:71], v[240:243], v[232:235], v[68:71]
	v_mfma_f32_16x16x32_bf16 v[64:67], v[248:251], v[232:235], v[64:67]
	ds_read_b128 v[232:235], v152 offset:56320
	s_barrier
	s_setprio 0
	global_load_lds_dwordx4 v[170:171], off
	v_lshl_add_u64 v[166:167], v[166:167], 0, s[94:95]
	s_mov_b32 m0, s48
	s_nop 0
	global_load_lds_dwordx4 v[166:167], off
	s_waitcnt vmcnt(8)
	s_setprio 1
	s_barrier
	s_waitcnt lgkmcnt(0)
	v_mfma_f32_16x16x32_bf16 v[60:63], v[158:161], v[180:183], v[60:63]
	v_mfma_f32_16x16x32_bf16 v[56:59], v[172:175], v[180:183], v[56:59]
	v_mfma_f32_16x16x32_bf16 v[52:55], v[158:161], v[212:215], v[52:55]
	v_mfma_f32_16x16x32_bf16 v[48:51], v[172:175], v[212:215], v[48:51]
	v_mfma_f32_16x16x32_bf16 v[44:47], v[158:161], v[220:223], v[44:47]
	v_mfma_f32_16x16x32_bf16 v[40:43], v[172:175], v[220:223], v[40:43]
	v_mfma_f32_16x16x32_bf16 v[36:39], v[158:161], v[228:231], v[36:39]
	v_mfma_f32_16x16x32_bf16 v[32:35], v[172:175], v[228:231], v[32:35]
	v_mfma_f32_16x16x32_bf16 v[60:63], v[162:165], v[208:211], v[60:63]
	v_mfma_f32_16x16x32_bf16 v[56:59], v[176:179], v[208:211], v[56:59]
	v_mfma_f32_16x16x32_bf16 v[52:55], v[162:165], v[216:219], v[52:55]
	v_mfma_f32_16x16x32_bf16 v[48:51], v[176:179], v[216:219], v[48:51]
	v_mfma_f32_16x16x32_bf16 v[44:47], v[162:165], v[224:227], v[44:47]
	v_mfma_f32_16x16x32_bf16 v[40:43], v[176:179], v[224:227], v[40:43]
	v_mfma_f32_16x16x32_bf16 v[36:39], v[162:165], v[232:235], v[36:39]
	v_mfma_f32_16x16x32_bf16 v[32:35], v[176:179], v[232:235], v[32:35]
	s_barrier
	s_setprio 0
	s_add_u32 s36, s36, 0x80080
	s_addc_u32 s37, s37, 0
	s_add_i32 s38, s38, s9
	v_lshl_add_u64 v[158:159], s[36:37], 0, v[130:131]
	s_mov_b32 m0, s38
	s_nop 0
	global_load_lds_dwordx4 v[158:159], off
	v_lshl_add_u64 v[158:159], s[36:37], 0, v[136:137]
	s_add_i32 m0, s38, 0x2000
	s_nop 0
	global_load_lds_dwordx4 v[158:159], off
	s_waitcnt vmcnt(6)
	s_setprio 1
	s_barrier
	v_mfma_f32_16x16x32_bf16 v[28:31], v[236:239], v[180:183], v[28:31]
	s_add_i32 s57, s57, 2
	v_mfma_f32_16x16x32_bf16 v[24:27], v[244:247], v[180:183], v[24:27]
	s_add_u32 s34, s34, 0x100
	ds_read_b128 v[180:183], v152
	v_mfma_f32_16x16x32_bf16 v[20:23], v[236:239], v[212:215], v[20:23]
	s_addc_u32 s35, s35, 0
	v_mfma_f32_16x16x32_bf16 v[16:19], v[244:247], v[212:215], v[16:19]
	s_cmp_gt_u32 s57, 29
	ds_read_b128 v[212:215], v152 offset:2048
	v_mfma_f32_16x16x32_bf16 v[12:15], v[236:239], v[220:223], v[12:15]
	v_mfma_f32_16x16x32_bf16 v[8:11], v[244:247], v[220:223], v[8:11]
	ds_read_b128 v[220:223], v152 offset:4096
	v_mfma_f32_16x16x32_bf16 v[4:7], v[236:239], v[228:231], v[4:7]
	v_mfma_f32_16x16x32_bf16 v[0:3], v[244:247], v[228:231], v[0:3]
	ds_read_b128 v[228:231], v152 offset:6144
	v_mfma_f32_16x16x32_bf16 v[28:31], v[240:243], v[208:211], v[28:31]
	v_mfma_f32_16x16x32_bf16 v[24:27], v[248:251], v[208:211], v[24:27]
	ds_read_b128 v[208:211], v152 offset:1024
	v_mfma_f32_16x16x32_bf16 v[20:23], v[240:243], v[216:219], v[20:23]
	v_mfma_f32_16x16x32_bf16 v[16:19], v[248:251], v[216:219], v[16:19]
	ds_read_b128 v[216:219], v152 offset:3072
	v_mfma_f32_16x16x32_bf16 v[12:15], v[240:243], v[224:227], v[12:15]
	v_mfma_f32_16x16x32_bf16 v[8:11], v[248:251], v[224:227], v[8:11]
	ds_read_b128 v[224:227], v152 offset:5120
	v_mfma_f32_16x16x32_bf16 v[4:7], v[240:243], v[232:235], v[4:7]
	v_mfma_f32_16x16x32_bf16 v[0:3], v[248:251], v[232:235], v[0:3]
	ds_read_b128 v[232:235], v152 offset:7168
	s_barrier
	s_setprio 0
	s_cbranch_scc0 .LBB0_1423
	s_waitcnt lgkmcnt(0)
	s_and_b64 vcc, exec, s[16:17]
	s_cbranch_vccz .LBB0_1426
	s_barrier

.LBB0_1521:
	s_add_u32 s26, s24, 0x80
	s_addc_u32 s27, s25, 0
	s_add_i32 s57, 0, 0x10000
	v_add_u32_e32 v147, s57, v145
	ds_read_b128 v[148:151], v147
	ds_read_b128 v[152:155], v147 offset:1024
	ds_read_b128 v[156:159], v147 offset:2048
	ds_read_b128 v[160:163], v147 offset:3072
	s_cmp_eq_u32 s56, 4
	s_cselect_b32 s29, s17, s27
	s_cselect_b32 s28, s21, s26
	s_cselect_b32 s27, s30, s35
	s_cselect_b32 s26, s31, s34
	v_lshl_add_u64 v[170:171], s[24:25], 0, v[142:143]
	s_add_i32 m0, s43, 0xc000
	s_nop 0
	global_load_lds_dwordx4 v[170:171], off
	v_lshl_add_u64 v[170:171], s[24:25], 0, v[140:141]
	s_add_i32 m0, s43, 0xe000
	s_nop 0
	global_load_lds_dwordx4 v[170:171], off
	s_waitcnt lgkmcnt(0)
	s_setprio 1
	s_barrier
	s_waitcnt lgkmcnt(0)
	v_mfma_f32_16x16x32_bf16 v[124:127], v[148:151], v[164:167], v[124:127]
	v_mfma_f32_16x16x32_bf16 v[120:123], v[156:159], v[164:167], v[120:123]
	v_mfma_f32_16x16x32_bf16 v[112:115], v[148:151], v[176:179], v[112:115]
	v_mfma_f32_16x16x32_bf16 v[104:107], v[156:159], v[176:179], v[104:107]
	v_mfma_f32_16x16x32_bf16 v[96:99], v[148:151], v[208:211], v[96:99]
	v_mfma_f32_16x16x32_bf16 v[88:91], v[156:159], v[208:211], v[88:91]
	v_mfma_f32_16x16x32_bf16 v[80:83], v[148:151], v[216:219], v[80:83]
	v_mfma_f32_16x16x32_bf16 v[72:75], v[156:159], v[216:219], v[72:75]
	v_mfma_f32_16x16x32_bf16 v[124:127], v[152:155], v[172:175], v[124:127]
	v_mfma_f32_16x16x32_bf16 v[120:123], v[160:163], v[172:175], v[120:123]
	v_mfma_f32_16x16x32_bf16 v[112:115], v[152:155], v[180:183], v[112:115]
	v_mfma_f32_16x16x32_bf16 v[104:107], v[160:163], v[180:183], v[104:107]
	v_mfma_f32_16x16x32_bf16 v[96:99], v[152:155], v[212:215], v[96:99]
	v_mfma_f32_16x16x32_bf16 v[88:91], v[160:163], v[212:215], v[88:91]
	v_mfma_f32_16x16x32_bf16 v[80:83], v[152:155], v[220:223], v[80:83]
	v_mfma_f32_16x16x32_bf16 v[72:75], v[160:163], v[220:223], v[72:75]
	s_barrier
	s_setprio 0
	s_add_i32 s60, 0, 0x14000
	s_add_i32 s57, s57, s42
	v_add_u32_e32 v147, s60, v145
	v_lshl_add_u64 v[170:171], s[26:27], 0, v[168:169]
	s_mov_b32 m0, s57
	ds_read_b128 v[224:227], v147
	ds_read_b128 v[228:231], v147 offset:1024
	ds_read_b128 v[232:235], v147 offset:2048
	ds_read_b128 v[236:239], v147 offset:3072
	global_load_lds_dwordx4 v[170:171], off
	v_lshl_add_u64 v[184:185], s[26:27], 0, v[132:133]
	s_add_i32 m0, s57, 0x2000
	s_nop 0
	global_load_lds_dwordx4 v[184:185], off
	s_setprio 1
	s_barrier
	s_waitcnt lgkmcnt(0)
	v_mfma_f32_16x16x32_bf16 v[116:119], v[224:227], v[164:167], v[116:119]
	s_mov_b32 m0, s43
	v_mfma_f32_16x16x32_bf16 v[108:111], v[232:235], v[164:167], v[108:111]
	v_lshl_add_u64 v[188:189], s[28:29], 0, v[128:129]
	ds_read_b128 v[164:167], v146 offset:16384
	v_mfma_f32_16x16x32_bf16 v[100:103], v[224:227], v[176:179], v[100:103]
	v_mfma_f32_16x16x32_bf16 v[92:95], v[232:235], v[176:179], v[92:95]
	ds_read_b128 v[176:179], v146 offset:18432
	v_mfma_f32_16x16x32_bf16 v[84:87], v[224:227], v[208:211], v[84:87]
	v_mfma_f32_16x16x32_bf16 v[76:79], v[232:235], v[208:211], v[76:79]
	ds_read_b128 v[208:211], v146 offset:20480
	v_mfma_f32_16x16x32_bf16 v[68:71], v[224:227], v[216:219], v[68:71]
	v_mfma_f32_16x16x32_bf16 v[64:67], v[232:235], v[216:219], v[64:67]
	ds_read_b128 v[216:219], v146 offset:22528
	v_mfma_f32_16x16x32_bf16 v[116:119], v[228:231], v[172:175], v[116:119]
	v_mfma_f32_16x16x32_bf16 v[108:111], v[236:239], v[172:175], v[108:111]
	ds_read_b128 v[172:175], v146 offset:17408
	v_mfma_f32_16x16x32_bf16 v[100:103], v[228:231], v[180:183], v[100:103]
	v_mfma_f32_16x16x32_bf16 v[92:95], v[236:239], v[180:183], v[92:95]
	ds_read_b128 v[180:183], v146 offset:19456
	v_mfma_f32_16x16x32_bf16 v[84:87], v[228:231], v[212:215], v[84:87]
	v_mfma_f32_16x16x32_bf16 v[76:79], v[236:239], v[212:215], v[76:79]
	ds_read_b128 v[212:215], v146 offset:21504
	v_mfma_f32_16x16x32_bf16 v[68:71], v[228:231], v[220:223], v[68:71]
	v_mfma_f32_16x16x32_bf16 v[64:67], v[236:239], v[220:223], v[64:67]
	ds_read_b128 v[220:223], v146 offset:23552
	s_barrier
	s_setprio 0
	global_load_lds_dwordx4 v[188:189], off
	v_lshl_add_u64 v[240:241], s[28:29], 0, v[134:135]
	s_mov_b32 m0, s44
	s_nop 0
	global_load_lds_dwordx4 v[240:241], off
	s_waitcnt vmcnt(8)
	s_setprio 1
	s_barrier
	s_waitcnt lgkmcnt(0)
	v_mfma_f32_16x16x32_bf16 v[60:63], v[148:151], v[164:167], v[60:63]
	v_mfma_f32_16x16x32_bf16 v[56:59], v[156:159], v[164:167], v[56:59]
	v_mfma_f32_16x16x32_bf16 v[40:43], v[148:151], v[176:179], v[40:43]
	v_mfma_f32_16x16x32_bf16 v[32:35], v[156:159], v[176:179], v[32:35]
	v_mfma_f32_16x16x32_bf16 v[16:19], v[148:151], v[208:211], v[16:19]
	v_mfma_f32_16x16x32_bf16 v[12:15], v[156:159], v[208:211], v[12:15]
	v_mfma_f32_16x16x32_bf16 v[4:7], v[148:151], v[216:219], v[4:7]
	v_mfma_f32_16x16x32_bf16 v[0:3], v[156:159], v[216:219], v[0:3]
	v_mfma_f32_16x16x32_bf16 v[60:63], v[152:155], v[172:175], v[60:63]
	v_mfma_f32_16x16x32_bf16 v[56:59], v[160:163], v[172:175], v[56:59]
	v_mfma_f32_16x16x32_bf16 v[40:43], v[152:155], v[180:183], v[40:43]
	v_mfma_f32_16x16x32_bf16 v[32:35], v[160:163], v[180:183], v[32:35]
	v_mfma_f32_16x16x32_bf16 v[16:19], v[152:155], v[212:215], v[16:19]
	v_mfma_f32_16x16x32_bf16 v[12:15], v[160:163], v[212:215], v[12:15]
	v_mfma_f32_16x16x32_bf16 v[4:7], v[152:155], v[220:223], v[4:7]
	v_mfma_f32_16x16x32_bf16 v[0:3], v[160:163], v[220:223], v[0:3]
	s_barrier
	s_setprio 0
	s_add_u32 s58, s26, 0x2000
	s_addc_u32 s59, s27, 0
	s_add_i32 s57, s60, s42
	v_lshl_add_u64 v[148:149], s[58:59], 0, v[168:169]
	s_mov_b32 m0, s57
	s_nop 0
	global_load_lds_dwordx4 v[148:149], off
	v_lshl_add_u64 v[148:149], s[58:59], 0, v[132:133]
	s_add_i32 m0, s57, 0x2000
	s_nop 0
	global_load_lds_dwordx4 v[148:149], off
	s_waitcnt vmcnt(6)
	s_setprio 1
	s_barrier
	v_mfma_f32_16x16x32_bf16 v[44:47], v[224:227], v[164:167], v[44:47]
	s_add_i32 s57, 0, 0x18000
	v_mfma_f32_16x16x32_bf16 v[36:39], v[232:235], v[164:167], v[36:39]
	v_add_u32_e32 v147, s57, v145
	ds_read_b128 v[164:167], v146 offset:32768
	v_mfma_f32_16x16x32_bf16 v[20:23], v[224:227], v[176:179], v[20:23]
	v_mfma_f32_16x16x32_bf16 v[8:11], v[232:235], v[176:179], v[8:11]
	ds_read_b128 v[176:179], v146 offset:34816
	v_mfma_f32_16x16x32_bf16 v[52:55], v[224:227], v[208:211], v[52:55]
	v_mfma_f32_16x16x32_bf16 v[48:51], v[232:235], v[208:211], v[48:51]
	ds_read_b128 v[208:211], v146 offset:36864
	v_mfma_f32_16x16x32_bf16 v[28:31], v[224:227], v[216:219], v[28:31]
	v_mfma_f32_16x16x32_bf16 v[24:27], v[232:235], v[216:219], v[24:27]
	ds_read_b128 v[216:219], v146 offset:38912
	v_mfma_f32_16x16x32_bf16 v[44:47], v[228:231], v[172:175], v[44:47]
	v_mfma_f32_16x16x32_bf16 v[36:39], v[236:239], v[172:175], v[36:39]
	ds_read_b128 v[172:175], v146 offset:33792
	v_mfma_f32_16x16x32_bf16 v[20:23], v[228:231], v[180:183], v[20:23]
	v_mfma_f32_16x16x32_bf16 v[8:11], v[236:239], v[180:183], v[8:11]
	ds_read_b128 v[180:183], v146 offset:35840
	v_mfma_f32_16x16x32_bf16 v[52:55], v[228:231], v[212:215], v[52:55]
	v_mfma_f32_16x16x32_bf16 v[48:51], v[236:239], v[212:215], v[48:51]
	ds_read_b128 v[212:215], v146 offset:37888
	v_mfma_f32_16x16x32_bf16 v[28:31], v[228:231], v[220:223], v[28:31]
	v_mfma_f32_16x16x32_bf16 v[24:27], v[236:239], v[220:223], v[24:27]
	ds_read_b128 v[220:223], v146 offset:39936
	s_barrier
	s_setprio 0
	ds_read_b128 v[148:151], v147
	ds_read_b128 v[152:155], v147 offset:1024
	ds_read_b128 v[156:159], v147 offset:2048
	ds_read_b128 v[160:163], v147 offset:3072
	s_mov_b32 m0, s45
	v_lshl_add_u64 v[224:225], s[28:29], 0, v[130:131]
	global_load_lds_dwordx4 v[224:225], off
	v_lshl_add_u64 v[224:225], s[28:29], 0, v[136:137]
	s_mov_b32 m0, s46
	s_nop 0
	global_load_lds_dwordx4 v[224:225], off
	s_waitcnt lgkmcnt(0)
	s_setprio 1
	s_barrier
	s_waitcnt lgkmcnt(0)
	v_mfma_f32_16x16x32_bf16 v[124:127], v[148:151], v[164:167], v[124:127]
	v_mfma_f32_16x16x32_bf16 v[120:123], v[156:159], v[164:167], v[120:123]
	v_mfma_f32_16x16x32_bf16 v[112:115], v[148:151], v[176:179], v[112:115]
	v_mfma_f32_16x16x32_bf16 v[104:107], v[156:159], v[176:179], v[104:107]
	v_mfma_f32_16x16x32_bf16 v[96:99], v[148:151], v[208:211], v[96:99]
	v_mfma_f32_16x16x32_bf16 v[88:91], v[156:159], v[208:211], v[88:91]
	v_mfma_f32_16x16x32_bf16 v[80:83], v[148:151], v[216:219], v[80:83]
	v_mfma_f32_16x16x32_bf16 v[72:75], v[156:159], v[216:219], v[72:75]
	v_mfma_f32_16x16x32_bf16 v[124:127], v[152:155], v[172:175], v[124:127]
	v_mfma_f32_16x16x32_bf16 v[120:123], v[160:163], v[172:175], v[120:123]
	v_mfma_f32_16x16x32_bf16 v[112:115], v[152:155], v[180:183], v[112:115]
	v_mfma_f32_16x16x32_bf16 v[104:107], v[160:163], v[180:183], v[104:107]
	v_mfma_f32_16x16x32_bf16 v[96:99], v[152:155], v[212:215], v[96:99]
	v_mfma_f32_16x16x32_bf16 v[88:91], v[160:163], v[212:215], v[88:91]
	v_mfma_f32_16x16x32_bf16 v[80:83], v[152:155], v[220:223], v[80:83]
	v_mfma_f32_16x16x32_bf16 v[72:75], v[160:163], v[220:223], v[72:75]
	s_barrier
	s_setprio 0
	s_add_i32 s28, 0, 0x1c000
	s_add_i32 s29, s57, s42
	v_add_u32_e32 v147, s28, v145
	v_lshl_add_u64 v[170:171], v[170:171], 0, s[94:95]
	s_mov_b32 m0, s29
	ds_read_b128 v[224:227], v147
	ds_read_b128 v[228:231], v147 offset:1024
	ds_read_b128 v[232:235], v147 offset:2048
	ds_read_b128 v[236:239], v147 offset:3072
	global_load_lds_dwordx4 v[170:171], off
	v_lshl_add_u64 v[170:171], v[184:185], 0, s[94:95]
	s_add_i32 m0, s29, 0x2000
	s_nop 0
	global_load_lds_dwordx4 v[170:171], off
	s_setprio 1
	s_barrier
	s_waitcnt lgkmcnt(0)
	v_mfma_f32_16x16x32_bf16 v[116:119], v[224:227], v[164:167], v[116:119]
	s_mov_b32 m0, s47
	v_mfma_f32_16x16x32_bf16 v[108:111], v[232:235], v[164:167], v[108:111]
	v_lshl_add_u64 v[170:171], v[188:189], 0, s[94:95]
	ds_read_b128 v[164:167], v146 offset:49152
	v_mfma_f32_16x16x32_bf16 v[100:103], v[224:227], v[176:179], v[100:103]
	v_mfma_f32_16x16x32_bf16 v[92:95], v[232:235], v[176:179], v[92:95]
	ds_read_b128 v[176:179], v146 offset:51200
	v_mfma_f32_16x16x32_bf16 v[84:87], v[224:227], v[208:211], v[84:87]
	v_mfma_f32_16x16x32_bf16 v[76:79], v[232:235], v[208:211], v[76:79]
	ds_read_b128 v[208:211], v146 offset:53248
	v_mfma_f32_16x16x32_bf16 v[68:71], v[224:227], v[216:219], v[68:71]
	v_mfma_f32_16x16x32_bf16 v[64:67], v[232:235], v[216:219], v[64:67]
	ds_read_b128 v[216:219], v146 offset:55296
	v_mfma_f32_16x16x32_bf16 v[116:119], v[228:231], v[172:175], v[116:119]
	v_mfma_f32_16x16x32_bf16 v[108:111], v[236:239], v[172:175], v[108:111]
	ds_read_b128 v[172:175], v146 offset:50176
	v_mfma_f32_16x16x32_bf16 v[100:103], v[228:231], v[180:183], v[100:103]
	v_mfma_f32_16x16x32_bf16 v[92:95], v[236:239], v[180:183], v[92:95]
	ds_read_b128 v[180:183], v146 offset:52224
	v_mfma_f32_16x16x32_bf16 v[84:87], v[228:231], v[212:215], v[84:87]
	v_mfma_f32_16x16x32_bf16 v[76:79], v[236:239], v[212:215], v[76:79]
	ds_read_b128 v[212:215], v146 offset:54272
	v_mfma_f32_16x16x32_bf16 v[68:71], v[228:231], v[220:223], v[68:71]
	v_mfma_f32_16x16x32_bf16 v[64:67], v[236:239], v[220:223], v[64:67]
	ds_read_b128 v[220:223], v146 offset:56320
	s_barrier
	s_setprio 0
	global_load_lds_dwordx4 v[170:171], off
	v_lshl_add_u64 v[170:171], v[240:241], 0, s[94:95]
	s_mov_b32 m0, s48
	s_nop 0
	global_load_lds_dwordx4 v[170:171], off
	s_waitcnt vmcnt(8)
	s_setprio 1
	s_barrier
	s_waitcnt lgkmcnt(0)
	v_mfma_f32_16x16x32_bf16 v[60:63], v[148:151], v[164:167], v[60:63]
	v_mfma_f32_16x16x32_bf16 v[56:59], v[156:159], v[164:167], v[56:59]
	v_mfma_f32_16x16x32_bf16 v[40:43], v[148:151], v[176:179], v[40:43]
	v_mfma_f32_16x16x32_bf16 v[32:35], v[156:159], v[176:179], v[32:35]
	v_mfma_f32_16x16x32_bf16 v[16:19], v[148:151], v[208:211], v[16:19]
	v_mfma_f32_16x16x32_bf16 v[12:15], v[156:159], v[208:211], v[12:15]
	v_mfma_f32_16x16x32_bf16 v[4:7], v[148:151], v[216:219], v[4:7]
	v_mfma_f32_16x16x32_bf16 v[0:3], v[156:159], v[216:219], v[0:3]
	v_mfma_f32_16x16x32_bf16 v[60:63], v[152:155], v[172:175], v[60:63]
	v_mfma_f32_16x16x32_bf16 v[56:59], v[160:163], v[172:175], v[56:59]
	v_mfma_f32_16x16x32_bf16 v[40:43], v[152:155], v[180:183], v[40:43]
	v_mfma_f32_16x16x32_bf16 v[32:35], v[160:163], v[180:183], v[32:35]
	v_mfma_f32_16x16x32_bf16 v[16:19], v[152:155], v[212:215], v[16:19]
	v_mfma_f32_16x16x32_bf16 v[12:15], v[160:163], v[212:215], v[12:15]
	v_mfma_f32_16x16x32_bf16 v[4:7], v[152:155], v[220:223], v[4:7]
	v_mfma_f32_16x16x32_bf16 v[0:3], v[160:163], v[220:223], v[0:3]
	s_barrier
	s_setprio 0
	s_add_u32 s26, s26, 0x2080
	s_addc_u32 s27, s27, 0
	s_add_i32 s28, s28, s42
	v_lshl_add_u64 v[148:149], s[26:27], 0, v[168:169]
	s_mov_b32 m0, s28
	s_nop 0
	global_load_lds_dwordx4 v[148:149], off
	v_lshl_add_u64 v[148:149], s[26:27], 0, v[132:133]
	s_add_i32 m0, s28, 0x2000
	s_nop 0
	global_load_lds_dwordx4 v[148:149], off
	s_waitcnt vmcnt(6)
	s_setprio 1
	s_barrier
	v_mfma_f32_16x16x32_bf16 v[44:47], v[224:227], v[164:167], v[44:47]
	s_add_i32 s56, s56, 2
	v_mfma_f32_16x16x32_bf16 v[36:39], v[232:235], v[164:167], v[36:39]
	s_add_u32 s24, s24, 0x100
	ds_read_b128 v[164:167], v146
	v_mfma_f32_16x16x32_bf16 v[20:23], v[224:227], v[176:179], v[20:23]
	s_addc_u32 s25, s25, 0
	v_mfma_f32_16x16x32_bf16 v[8:11], v[232:235], v[176:179], v[8:11]
	s_add_u32 s34, s34, 0x100
	ds_read_b128 v[176:179], v146 offset:2048
	v_mfma_f32_16x16x32_bf16 v[52:55], v[224:227], v[208:211], v[52:55]
	s_addc_u32 s35, s35, 0
	v_mfma_f32_16x16x32_bf16 v[48:51], v[232:235], v[208:211], v[48:51]
	s_cmp_gt_u32 s56, 5
	ds_read_b128 v[208:211], v146 offset:4096
	v_mfma_f32_16x16x32_bf16 v[28:31], v[224:227], v[216:219], v[28:31]
	v_mfma_f32_16x16x32_bf16 v[24:27], v[232:235], v[216:219], v[24:27]
	ds_read_b128 v[216:219], v146 offset:6144
	v_mfma_f32_16x16x32_bf16 v[44:47], v[228:231], v[172:175], v[44:47]
	v_mfma_f32_16x16x32_bf16 v[36:39], v[236:239], v[172:175], v[36:39]
	ds_read_b128 v[172:175], v146 offset:1024
	v_mfma_f32_16x16x32_bf16 v[20:23], v[228:231], v[180:183], v[20:23]
	v_mfma_f32_16x16x32_bf16 v[8:11], v[236:239], v[180:183], v[8:11]
	ds_read_b128 v[180:183], v146 offset:3072
	v_mfma_f32_16x16x32_bf16 v[52:55], v[228:231], v[212:215], v[52:55]
	v_mfma_f32_16x16x32_bf16 v[48:51], v[236:239], v[212:215], v[48:51]
	ds_read_b128 v[212:215], v146 offset:5120
	v_mfma_f32_16x16x32_bf16 v[28:31], v[228:231], v[220:223], v[28:31]
	v_mfma_f32_16x16x32_bf16 v[24:27], v[236:239], v[220:223], v[24:27]
	ds_read_b128 v[220:223], v146 offset:7168
	s_barrier
	s_setprio 0
	s_cbranch_scc0 .LBB0_1521
	s_waitcnt lgkmcnt(0)
	s_and_b64 vcc, exec, s[6:7]
	s_cbranch_vccz .LBB0_1524
	s_barrier
